# baseline (speedup 1.0000x reference)
.LBB3_32:
	s_barrier
	v_accvgpr_read_b32 v140, a72
	v_lshlrev_b64 v[142:143], 2, v[94:95]
	v_lshlrev_b64 v[144:145], 2, v[96:97]
	v_lshlrev_b64 v[146:147], 2, v[98:99]
	v_lshlrev_b64 v[148:149], 2, v[100:101]
	s_add_u32 s52, s10, 0x800000
	s_addc_u32 s53, s11, 0
	v_add_u32_e32 v150, 0x0, v91
	v_lshl_add_u64 v[152:153], s[52:53], 0, v[146:147]
	s_nop 0
	v_readfirstlane_b32 s44, v150
	s_mov_b32 m0, s44
	s_nop 0
	global_load_lds_dwordx4 v[152:153], off nt
	v_add_u32_e32 v150, 0x0, v119
	v_lshl_add_u64 v[152:153], s[52:53], 0, v[148:149]
	s_nop 0
	v_readfirstlane_b32 s44, v150
	s_mov_b32 m0, s44
	s_nop 0
	global_load_lds_dwordx4 v[152:153], off nt
	s_add_u32 s52, s10, 0xc00000
	s_addc_u32 s53, s11, 0
	v_add_u32_e32 v150, 0x7000, v140
	v_lshl_add_u64 v[152:153], s[52:53], 0, v[142:143]
	s_nop 0
	v_readfirstlane_b32 s44, v150
	s_mov_b32 m0, s44
	s_nop 0
	global_load_lds_dwordx4 v[152:153], off nt
	v_add_u32_e32 v150, 0x7000, v90
	v_lshl_add_u64 v[152:153], s[52:53], 0, v[144:145]
	s_nop 0
	v_readfirstlane_b32 s44, v150
	s_mov_b32 m0, s44
	s_nop 0
	global_load_lds_dwordx4 v[152:153], off nt
	v_add_u32_e32 v150, 0x7000, v91
	v_lshl_add_u64 v[152:153], s[52:53], 0, v[146:147]
	s_nop 0
	v_readfirstlane_b32 s44, v150
	s_mov_b32 m0, s44
	s_nop 0
	global_load_lds_dwordx4 v[152:153], off nt
	v_add_u32_e32 v150, 0x7000, v119
	v_lshl_add_u64 v[152:153], s[52:53], 0, v[148:149]
	s_nop 0
	v_readfirstlane_b32 s44, v150
	s_mov_b32 m0, s44
	s_nop 0
	global_load_lds_dwordx4 v[152:153], off nt
	s_add_u32 s52, s10, 0x1000000
	s_addc_u32 s53, s11, 0
	v_add_u32_e32 v150, 0xe000, v140
	v_lshl_add_u64 v[152:153], s[52:53], 0, v[142:143]
	s_nop 0
	v_readfirstlane_b32 s44, v150
	s_mov_b32 m0, s44
	s_nop 0
	global_load_lds_dwordx4 v[152:153], off nt
	v_add_u32_e32 v150, 0xe000, v90
	v_lshl_add_u64 v[152:153], s[52:53], 0, v[144:145]
	s_nop 0
	v_readfirstlane_b32 s44, v150
	s_mov_b32 m0, s44
	s_nop 0
	global_load_lds_dwordx4 v[152:153], off nt
	v_add_u32_e32 v150, 0xe000, v91
	v_lshl_add_u64 v[152:153], s[52:53], 0, v[146:147]
	s_nop 0
	v_readfirstlane_b32 s44, v150
	s_mov_b32 m0, s44
	s_nop 0
	global_load_lds_dwordx4 v[152:153], off nt
	v_add_u32_e32 v150, 0xe000, v119
	v_lshl_add_u64 v[152:153], s[52:53], 0, v[148:149]
	s_nop 0
	v_readfirstlane_b32 s44, v150
	s_mov_b32 m0, s44
	s_nop 0
	global_load_lds_dwordx4 v[152:153], off nt
	v_lshl_add_u32 v0, v120, 5, s22
	v_or_b32_e32 v1, s23, v121
	s_movk_i32 s0, 0x7f
	v_lshl_or_b32 v7, v93, 1, v0
	s_movk_i32 s1, 0x7e
	s_nop 15
	s_nop 15
	v_cmp_eq_u32_e64 s[4:5], s1, v7
	s_nop 7
	v_cmp_gt_u32_e32 vcc, s0, v1
	v_accvgpr_read_b32 v5, a14
	v_cmp_eq_u32_e64 s[0:1], 0, v1
	v_or_b32_e32 v4, v93, v7
	v_cmp_eq_u32_e64 s[2:3], 0, v4
	v_cndmask_b32_e64 v14, v5, 0, s[0:1]
	v_accvgpr_read_b32 v5, a13
	v_cndmask_b32_e64 v22, v5, 0, s[0:1]
	v_accvgpr_read_b32 v5, a12
	v_cndmask_b32_e64 v116, v5, 0, s[0:1]
	v_accvgpr_read_b32 v5, a49
	v_cndmask_b32_e32 v16, 0, v5, vcc
	v_accvgpr_read_b32 v5, a48
	v_cndmask_b32_e32 v28, 0, v5, vcc
	v_accvgpr_read_b32 v5, a30
	v_cndmask_b32_e64 v10, v5, 0, s[0:1]
	v_accvgpr_read_b32 v5, a29
	v_cndmask_b32_e64 v24, v5, 0, s[0:1]
	v_accvgpr_read_b32 v5, a28
	v_cndmask_b32_e64 v42, v5, 0, s[0:1]
	v_accvgpr_read_b32 v5, a57
	v_cndmask_b32_e32 v20, 0, v5, vcc
	v_accvgpr_read_b32 v5, a56
	v_cndmask_b32_e32 v38, 0, v5, vcc
	v_accvgpr_read_b32 v5, a6
	v_cndmask_b32_e64 v15, v5, 0, s[0:1]
	v_accvgpr_read_b32 v5, a5
	v_cndmask_b32_e64 v23, v5, 0, s[0:1]
	v_accvgpr_read_b32 v5, a4
	v_cndmask_b32_e64 v117, v5, 0, s[0:1]
	v_accvgpr_read_b32 v5, a41
	v_cndmask_b32_e32 v17, 0, v5, vcc
	v_accvgpr_read_b32 v5, a40
	v_cndmask_b32_e32 v29, 0, v5, vcc
	v_accvgpr_read_b32 v5, a17
	v_cndmask_b32_e64 v37, v5, 0, s[0:1]
	v_accvgpr_read_b32 v5, a16
	v_cndmask_b32_e64 v47, v5, 0, s[0:1]
	v_accvgpr_read_b32 v5, a52
	v_cndmask_b32_e32 v45, 0, v5, vcc
	v_accvgpr_read_b32 v5, a68
	v_cndmask_b32_e32 v12, 0, v5, vcc
	v_accvgpr_read_b32 v5, a0
	s_or_b64 s[8:9], s[2:3], s[0:1]
	v_cmp_eq_u32_e64 s[6:7], 15, v93
	v_accvgpr_read_b32 v11, a8
	v_cndmask_b32_e64 v112, v5, 0, s[8:9]
	v_accvgpr_read_b32 v4, a67
	v_mov_b32_e32 v5, 0x90
	s_and_b64 s[4:5], s[6:7], s[4:5]
	v_mov_b64_e32 v[40:41], v[16:17]
	v_cndmask_b32_e64 v16, v11, 0, s[2:3]
	v_cndmask_b32_e64 v11, 12, v5, s[6:7]
	v_cndmask_b32_e64 v61, v4, 0, s[4:5]
	v_accvgpr_read_b32 v4, a61
	s_or_b64 s[6:7], s[4:5], s[0:1]
	v_cndmask_b32_e64 v87, v4, 0, s[6:7]
	v_accvgpr_read_b32 v4, a60
	v_cndmask_b32_e64 v86, v4, 0, s[6:7]
	v_accvgpr_read_b32 v4, a65
	v_cndmask_b32_e64 v5, v4, 0, s[4:5]
	v_accvgpr_read_b32 v4, a64
	v_cndmask_b32_e64 v4, v4, 0, s[4:5]
	s_lshl_b32 s14, s18, 2
	v_mov_b64_e32 v[32:33], v[4:5]
	v_lshl_or_b32 v4, v122, 18, s14
	v_mov_b32_e32 v5, 0
	v_mov_b64_e32 v[62:63], v[14:15]
	v_lshl_add_u64 v[14:15], s[12:13], 0, v[4:5]
	v_lshlrev_b32_e32 v4, 7, v1
	v_lshl_add_u64 v[14:15], v[4:5], 2, v[14:15]
	v_lshlrev_b32_e32 v4, 2, v7
	v_mul_u32_u24_e32 v1, 24, v122
	v_lshl_add_u64 v[54:55], v[14:15], 0, v[4:5]
	v_mbcnt_lo_u32_b32 v138, -1, 0
	v_mbcnt_hi_u32_b32 v138, -1, v138
	v_and_b32_e32 v138, 1, v138
	v_mul_u32_u24_e32 v138, 0xfff8, v138
	v_add_u32_e32 v138, 0xffff0000, v138
	v_mov_b32_e32 v139, -1
	v_lshl_add_u64 v[134:135], v[54:55], 0, v[138:139]
	s_mov_b32 s28, 0x55555555
	s_mov_b32 s29, 0x55555555
	s_mov_b32 s30, 0xaaaaaaaa
	s_mov_b32 s31, 0xaaaaaaaa
	v_or_b32_e32 v1, v1, v121
	v_lshlrev_b32_e32 v4, 7, v120
	s_movk_i32 s12, 0x120
	v_mad_u32_u24 v1, v1, s12, v4
	s_add_u32 s12, s10, 0x800000
	v_accvgpr_read_b32 v7, a72
	v_mov_b64_e32 v[80:81], v[28:29]
	s_addc_u32 s13, s11, 0
	v_lshlrev_b64 v[28:29], 2, v[94:95]
	v_readfirstlane_b32 s14, v7
	v_add_u32_e32 v7, 0, v90
	v_lshl_add_u64 v[4:5], s[12:13], 0, v[28:29]
	s_mov_b32 m0, s14
	v_lshlrev_b64 v[30:31], 2, v[96:97]
	v_readfirstlane_b32 s14, v7
	v_mov_b32_e32 v14, v7
	v_add_u32_e32 v7, 0, v91
	s_waitcnt lgkmcnt(0)
	v_lshlrev_b64 v[56:57], 2, v[98:99]
	v_mov_b32_e32 v19, v7
	v_lshlrev_b64 v[58:59], 2, v[100:101]
	v_add_u32_e32 v7, 0, v119
	v_accvgpr_read_b32 v25, a72
	v_mov_b32_e32 v21, v7
	v_lshl_add_u32 v15, v93, 3, v1
	v_add_u32_e32 v1, v1, v11
	s_waitcnt vmcnt(16)
	v_accvgpr_write_b32 a12, v14
	v_mov_b64_e32 v[124:125], v[56:57]
	v_accvgpr_write_b32 a13, v19
	v_mov_b64_e32 v[126:127], v[58:59]
	v_accvgpr_write_b32 a16, v21
	s_waitcnt lgkmcnt(0)
	s_barrier
	v_add_u32_e32 v14, 0x16010, v15
	v_mov_b32_e32 v122, v15
	v_add_u32_e32 v15, 0x16000, v1
	ds_read_b64 v[64:65], v14
	ds_read_b64 v[66:67], v14 offset:288
	ds_read_b64 v[68:69], v14 offset:576
	ds_read_b64 v[76:77], v14 offset:1728
	ds_read_b64 v[78:79], v14 offset:2016
	ds_read_b64 v[4:5], v14 offset:2304
	ds_read_b64 v[84:85], v14 offset:3456
	ds_read_b64 v[74:75], v14 offset:3744
	ds_read_b64 v[88:89], v14 offset:4032
	ds_read_b64 v[100:101], v14 offset:5184
	ds_read_b64 v[106:107], v14 offset:5472
	ds_read_b64 v[120:121], v14 offset:5760
	ds_read_b32 v43, v15
	ds_read_b32 v19, v15 offset:288
	ds_read_b32 v39, v15 offset:576
	ds_read_b32 v25, v15 offset:1728
	ds_read_b32 v7, v15 offset:2016
	ds_read_b32 v21, v15 offset:2304
	ds_read_b32 v11, v15 offset:3456
	ds_read_b32 v35, v15 offset:3744
	ds_read_b32 v59, v15 offset:4032
	ds_read_b32 v57, v15 offset:5184
	ds_read_b32 v51, v15 offset:5472
	ds_read_b32 v49, v15 offset:5760
	s_waitcnt lgkmcnt(0)
	v_accvgpr_read_b32 v8, a26
	v_mov_b32_e32 v46, v43
	v_mov_b32_e32 v113, v65
	v_mov_b32_e32 v26, v19
	v_mov_b32_dpp v46, v65 row_shr:1 row_mask:0xf bank_mask:0xf
	v_pk_mul_f32 v[70:71], v[112:113], v[46:47]
	v_accvgpr_read_b32 v9, a22
	v_accvgpr_read_b32 v27, a36
	v_mov_b32_dpp v43, v64 row_shl:1 row_mask:0xf bank_mask:0xf
	v_mov_b32_dpp v26, v67 row_shr:1 row_mask:0xf bank_mask:0xf
	v_pk_fma_f32 v[70:71], v[64:65], v[116:117], v[70:71] op_sel_hi:[0,1,1]
	v_pk_mov_b32 v[64:65], v[64:65], v[86:87] op_sel:[1,0]
	v_mov_b32_e32 v17, v67
	v_mov_b64_e32 v[102:103], v[8:9]
	v_accvgpr_read_b32 v8, a25
	v_accvgpr_read_b32 v114, a24
	v_accvgpr_read_b32 v9, a21
	v_accvgpr_read_b32 v115, a20
	v_accvgpr_read_b32 v2, a32
	v_mov_b64_e32 v[82:83], v[30:31]
	v_pk_fma_f32 v[70:71], v[64:65], v[42:43], v[70:71]
	v_pk_mul_f32 v[64:65], v[16:17], v[26:27]
	v_mov_b64_e32 v[30:31], v[32:33]
	v_accvgpr_read_b32 v18, a44
	v_mov_b64_e32 v[104:105], v[8:9]
	v_cndmask_b32_e32 v9, 0, v2, vcc
	v_accvgpr_write_b32 a4, v14
	v_mov_b32_dpp v19, v66 row_shl:1 row_mask:0xf bank_mask:0xf
	v_pk_fma_f32 v[64:65], v[66:67], v[114:115], v[64:65] op_sel_hi:[0,1,1]
	v_pk_mov_b32 v[66:67], v[66:67], v[30:31] op_sel:[1,0]
	v_accvgpr_read_b32 v14, a69
	v_mov_b32_e32 v44, v39
	v_mov_b32_e32 v60, v1
	v_pk_fma_f32 v[66:67], v[66:67], v[18:19], v[64:65]
	v_cndmask_b32_e32 v14, 0, v14, vcc
	v_cndmask_b32_e64 v0, v9, 0, s[2:3]
	v_mov_b32_dpp v44, v69 row_shr:1 row_mask:0xf bank_mask:0xf
	v_pk_add_f32 v[70:71], v[70:71], 0 op_sel_hi:[1,0]
	v_mov_b32_e32 v1, v69
	v_accvgpr_write_b32 a0, v15
	v_cndmask_b32_e64 v15, v14, 0, s[4:5]
	v_cndmask_b32_e64 v14, v12, 0, s[4:5]
	v_pk_add_f32 v[66:67], v[70:71], v[66:67]
	v_pk_mul_f32 v[70:71], v[0:1], v[44:45]
	v_mov_b32_dpp v39, v68 row_shl:1 row_mask:0xf bank_mask:0xf
	v_pk_fma_f32 v[70:71], v[68:69], v[80:81], v[70:71] op_sel_hi:[0,1,1]
	v_pk_mov_b32 v[68:69], v[68:69], v[14:15] op_sel:[1,0]
	v_accvgpr_read_b32 v9, a1
	v_pk_fma_f32 v[68:69], v[68:69], v[38:39], v[70:71]
	v_mov_b32_e32 v36, v25
	v_cndmask_b32_e64 v64, v9, 0, s[8:9]
	v_pk_add_f32 v[66:67], v[66:67], v[68:69]
	v_mov_b32_dpp v36, v77 row_shr:1 row_mask:0xf bank_mask:0xf
	v_mov_b32_e32 v65, v77
	v_mov_b64_e32 v[108:109], v[22:23]
	v_accvgpr_read_b32 v9, a9
	v_mov_b32_e32 v128, v66
	v_mov_b32_e32 v129, v67
	v_mov_b32_e32 v12, v7
	v_pk_mul_f32 v[66:67], v[64:65], v[36:37]
	v_accvgpr_read_b32 v13, a37
	v_mov_b64_e32 v[72:73], v[28:29]
	v_cndmask_b32_e64 v28, v9, 0, s[2:3]
	v_mov_b32_dpp v25, v76 row_shl:1 row_mask:0xf bank_mask:0xf
	v_mov_b32_dpp v12, v79 row_shr:1 row_mask:0xf bank_mask:0xf
	v_pk_fma_f32 v[66:67], v[76:77], v[108:109], v[66:67] op_sel_hi:[0,1,1]
	v_mov_b32_e32 v76, v77
	v_mov_b32_e32 v77, v87
	v_mov_b32_e32 v29, v79
	v_pk_fma_f32 v[66:67], v[76:77], v[24:25], v[66:67]
	v_pk_mul_f32 v[76:77], v[28:29], v[12:13]
	v_accvgpr_read_b32 v6, a45
	v_accvgpr_read_b32 v2, a33
	v_mov_b32_dpp v7, v78 row_shl:1 row_mask:0xf bank_mask:0xf
	v_pk_fma_f32 v[76:77], v[78:79], v[104:105], v[76:77] op_sel_hi:[0,1,1]
	v_mov_b32_e32 v78, v79
	v_mov_b32_e32 v79, v31
	v_cndmask_b32_e32 v2, 0, v2, vcc
	v_accvgpr_read_b32 v50, a53
	v_pk_fma_f32 v[76:77], v[78:79], v[6:7], v[76:77]
	v_mov_b32_e32 v78, v21
	v_accvgpr_write_b32 a44, v80
	v_cndmask_b32_e32 v79, 0, v50, vcc
	v_cndmask_b32_e64 v52, v2, 0, s[2:3]
	v_mov_b32_dpp v78, v5 row_shr:1 row_mask:0xf bank_mask:0xf
	v_pk_add_f32 v[66:67], v[66:67], 0 op_sel_hi:[1,0]
	v_mov_b32_e32 v53, v5
	v_accvgpr_write_b32 a45, v81
	v_accvgpr_write_b32 a21, v15
	v_pk_add_f32 v[80:81], v[66:67], v[76:77]
	v_pk_mul_f32 v[66:67], v[52:53], v[78:79]
	v_accvgpr_write_b32 a24, v40
	v_accvgpr_read_b32 v2, a2
	v_mov_b32_dpp v21, v4 row_shl:1 row_mask:0xf bank_mask:0xf
	v_pk_fma_f32 v[66:67], v[4:5], v[40:41], v[66:67] op_sel_hi:[0,1,1]
	v_accvgpr_write_b32 a25, v41
	v_mov_b32_e32 v4, v5
	v_accvgpr_read_b32 v5, a21
	v_cndmask_b32_e64 v40, v2, 0, s[8:9]
	v_accvgpr_read_b32 v2, a62
	v_accvgpr_read_b32 v8, a18
	v_accvgpr_read_b32 v48, a63
	v_accvgpr_write_b32 a20, v14
	v_accvgpr_write_b32 a41, v23
	v_pk_fma_f32 v[4:5], v[4:5], v[20:21], v[66:67]
	s_mov_b64 s[12:13], 0x10000
	v_cndmask_b32_e64 v14, v2, 0, s[6:7]
	v_mov_b32_e32 v76, v11
	v_accvgpr_read_b32 v2, a10
	v_accvgpr_write_b32 a40, v22
	v_cndmask_b32_e64 v15, v48, 0, s[6:7]
	v_cndmask_b32_e64 v77, v8, 0, s[0:1]
	v_pk_add_f32 v[4:5], v[80:81], v[4:5]
	v_lshl_add_u64 v[136:137], v[134:135], 0, s[12:13]
	v_mov_b32_dpp v76, v85 row_shr:1 row_mask:0xf bank_mask:0xf
	v_mov_b32_e32 v41, v85
	v_cndmask_b32_e64 v22, v2, 0, s[2:3]
	v_mov_b32_e32 v2, v35
	v_accvgpr_read_b32 v1, a50
	v_accvgpr_read_b32 v3, a38
	s_mov_b64 s[32:33], vcc
	s_nop 1
	s_mov_b64 vcc, s[28:29]
	s_nop 0
	v_cndmask_b32_dpp v130, v4, v128, vcc quad_perm:[1,0,3,2] row_mask:0xf bank_mask:0xf
	v_cndmask_b32_dpp v131, v5, v129, vcc quad_perm:[1,0,3,2] row_mask:0xf bank_mask:0xf
	s_mov_b64 vcc, s[30:31]
	s_nop 0
	v_cndmask_b32_dpp v132, v128, v4, vcc quad_perm:[1,0,3,2] row_mask:0xf bank_mask:0xf
	v_cndmask_b32_dpp v133, v129, v5, vcc quad_perm:[1,0,3,2] row_mask:0xf bank_mask:0xf
	global_store_dwordx4 v[136:137], v[130:133], off sc0 sc1 nt
	s_nop 1
	s_mov_b64 vcc, s[32:33]
	v_mov_b64_e32 v[8:9], v[14:15]
	v_pk_mul_f32 v[4:5], v[40:41], v[76:77]
	v_mov_b64_e32 v[66:67], v[62:63]
	v_mov_b32_dpp v2, v75 row_shr:1 row_mask:0xf bank_mask:0xf
	v_mov_b32_e32 v23, v75
	v_cndmask_b32_e32 v62, 0, v1, vcc
	v_accvgpr_read_b32 v1, a42
	v_mov_b32_dpp v11, v84 row_shl:1 row_mask:0xf bank_mask:0xf
	v_pk_fma_f32 v[4:5], v[84:85], v[66:67], v[4:5] op_sel_hi:[0,1,1]
	v_pk_mov_b32 v[80:81], v[84:85], v[8:9] op_sel:[1,0]
	v_pk_mul_f32 v[84:85], v[22:23], v[2:3]
	v_accvgpr_read_b32 v2, a58
	v_cndmask_b32_e32 v63, 0, v1, vcc
	v_accvgpr_read_b32 v1, a70
	v_pk_fma_f32 v[80:81], v[80:81], v[10:11], v[4:5]
	v_accvgpr_read_b32 v4, a66
	v_cndmask_b32_e32 v58, 0, v2, vcc
	v_cndmask_b32_e32 v1, 0, v1, vcc
	v_accvgpr_read_b32 v2, a71
	v_cndmask_b32_e64 v8, v4, 0, s[4:5]
	v_cndmask_b32_e32 v2, 0, v2, vcc
	v_cndmask_b32_e64 v4, v1, 0, s[4:5]
	v_accvgpr_read_b32 v1, a34
	v_mov_b32_e32 v9, v61
	v_cndmask_b32_e64 v5, v2, 0, s[4:5]
	v_cndmask_b32_e32 v1, 0, v1, vcc
	v_accvgpr_read_b32 v2, a54
	v_mov_b32_e32 v92, v59
	v_accvgpr_read_b32 v34, a46
	v_mov_b32_dpp v35, v74 row_shl:1 row_mask:0xf bank_mask:0xf
	v_pk_fma_f32 v[84:85], v[74:75], v[102:103], v[84:85] op_sel_hi:[0,1,1]
	v_pk_mov_b32 v[74:75], v[74:75], v[8:9] op_sel:[1,0]
	v_cndmask_b32_e32 v93, 0, v2, vcc
	v_mov_b32_dpp v92, v89 row_shr:1 row_mask:0xf bank_mask:0xf
	v_cndmask_b32_e64 v96, v1, 0, s[2:3]
	v_mov_b32_e32 v97, v89
	v_accvgpr_read_b32 v1, a31
	v_pk_fma_f32 v[74:75], v[74:75], v[34:35], v[84:85]
	v_pk_mul_f32 v[84:85], v[96:97], v[92:93]
	v_accvgpr_write_b32 a8, v62
	v_cndmask_b32_e64 v56, v1, 0, s[0:1]
	v_accvgpr_read_b32 v1, a15
	v_pk_fma_f32 v[84:85], v[88:89], v[62:63], v[84:85] op_sel_hi:[0,1,1]
	v_accvgpr_write_b32 a9, v63
	v_cndmask_b32_e64 v62, v1, 0, s[0:1]
	v_accvgpr_read_b32 v1, a7
	v_cndmask_b32_e64 v63, v1, 0, s[0:1]
	v_accvgpr_read_b32 v1, a19
	v_pk_add_f32 v[80:81], v[80:81], 0 op_sel_hi:[1,0]
	v_mov_b32_dpp v59, v88 row_shl:1 row_mask:0xf bank_mask:0xf
	v_pk_mov_b32 v[88:89], v[88:89], v[4:5] op_sel:[1,0]
	v_cndmask_b32_e64 v95, v1, 0, s[0:1]
	v_accvgpr_read_b32 v1, a3
	v_accvgpr_write_b32 a36, v104
	v_pk_add_f32 v[80:81], v[80:81], v[74:75]
	v_pk_fma_f32 v[84:85], v[88:89], v[58:59], v[84:85]
	v_mov_b32_e32 v94, v57
	v_cndmask_b32_e64 v98, v1, 0, s[8:9]
	v_accvgpr_read_b32 v1, a11
	v_accvgpr_write_b32 a37, v105
	v_accvgpr_write_b32 a32, v102
	v_pk_add_f32 v[80:81], v[80:81], v[84:85]
	s_mov_b64 s[4:5], 0x20000
	v_mov_b32_dpp v94, v101 row_shr:1 row_mask:0xf bank_mask:0xf
	v_mov_b32_e32 v99, v101
	v_cndmask_b32_e64 v104, v1, 0, s[2:3]
	v_accvgpr_read_b32 v1, a59
	v_accvgpr_write_b32 a29, v15
	v_accvgpr_write_b32 a33, v103
	v_accvgpr_write_b32 a49, v5
	v_lshl_add_u64 v[84:85], v[54:55], 0, s[4:5]
	v_mov_b32_e32 v128, v80
	v_mov_b32_e32 v129, v81
	v_pk_mul_f32 v[80:81], v[98:99], v[94:95]
	v_mov_b32_e32 v102, v51
	v_cndmask_b32_e32 v48, 0, v1, vcc
	v_accvgpr_read_b32 v1, a51
	v_accvgpr_write_b32 a48, v4
	v_mov_b32_dpp v57, v100 row_shl:1 row_mask:0xf bank_mask:0xf
	v_pk_fma_f32 v[80:81], v[100:101], v[62:63], v[80:81] op_sel_hi:[0,1,1]
	v_mov_b32_e32 v84, v101
	v_accvgpr_read_b32 v85, a29
	v_accvgpr_read_b32 v103, a39
	v_mov_b32_dpp v102, v107 row_shr:1 row_mask:0xf bank_mask:0xf
	v_mov_b32_e32 v105, v107
	v_cndmask_b32_e32 v4, 0, v1, vcc
	v_accvgpr_read_b32 v1, a43
	v_pk_fma_f32 v[80:81], v[84:85], v[56:57], v[80:81]
	v_accvgpr_read_b32 v30, a27
	v_accvgpr_read_b32 v31, a23
	v_pk_mul_f32 v[84:85], v[104:105], v[102:103]
	v_cndmask_b32_e32 v5, 0, v1, vcc
	v_accvgpr_read_b32 v1, a35
	v_accvgpr_read_b32 v50, a47
	v_mov_b32_dpp v51, v106 row_shl:1 row_mask:0xf bank_mask:0xf
	v_pk_fma_f32 v[84:85], v[106:107], v[30:31], v[84:85] op_sel_hi:[0,1,1]
	v_mov_b32_e32 v106, v107
	v_mov_b32_e32 v107, v9
	v_cndmask_b32_e32 v1, 0, v1, vcc
	v_accvgpr_read_b32 v2, a55
	v_mov_b32_e32 v108, v49
	v_pk_fma_f32 v[84:85], v[106:107], v[50:51], v[84:85]
	v_pk_add_f32 v[80:81], v[80:81], 0 op_sel_hi:[1,0]
	v_cndmask_b32_e32 v109, 0, v2, vcc
	v_mov_b32_dpp v108, v121 row_shr:1 row_mask:0xf bank_mask:0xf
	v_cndmask_b32_e64 v110, v1, 0, s[2:3]
	v_mov_b32_e32 v111, v121
	v_pk_add_f32 v[80:81], v[80:81], v[84:85]
	v_pk_mul_f32 v[84:85], v[110:111], v[108:109]
	v_mov_b32_dpp v49, v120 row_shl:1 row_mask:0xf bank_mask:0xf
	v_pk_fma_f32 v[84:85], v[120:121], v[4:5], v[84:85] op_sel_hi:[0,1,1]
	v_mov_b32_e32 v120, v121
	v_accvgpr_read_b32 v121, a49
	v_pk_fma_f32 v[84:85], v[120:121], v[48:49], v[84:85]
	s_mov_b64 s[0:1], 0x30000
	v_pk_add_f32 v[80:81], v[80:81], v[84:85]
	v_lshl_add_u64 v[136:137], v[134:135], 0, s[0:1]
	v_add_u32_e32 v1, s17, v118
	s_add_u32 s0, s10, 0x1400000
	s_mov_b64 s[32:33], vcc
	s_nop 1
	s_mov_b64 vcc, s[28:29]
	s_nop 0
	v_cndmask_b32_dpp v130, v80, v128, vcc quad_perm:[1,0,3,2] row_mask:0xf bank_mask:0xf
	v_cndmask_b32_dpp v131, v81, v129, vcc quad_perm:[1,0,3,2] row_mask:0xf bank_mask:0xf
	s_mov_b64 vcc, s[30:31]
	s_nop 0
	v_cndmask_b32_dpp v132, v128, v80, vcc quad_perm:[1,0,3,2] row_mask:0xf bank_mask:0xf
	v_cndmask_b32_dpp v133, v129, v81, vcc quad_perm:[1,0,3,2] row_mask:0xf bank_mask:0xf
	global_store_dwordx4 v[136:137], v[130:133], off sc0 sc1 nt
	s_nop 1
	s_mov_b64 vcc, s[32:33]
	v_readfirstlane_b32 s2, v1
	s_addc_u32 s1, s11, 0
	v_add_u32_e32 v1, s17, v90
	s_waitcnt vmcnt(12)
	v_lshl_add_u64 v[80:81], s[0:1], 0, v[72:73]
	s_mov_b32 m0, s2
	v_readfirstlane_b32 s2, v1
	v_mov_b64_e32 v[74:75], v[82:83]
	v_add_u32_e32 v1, s17, v91
	s_waitcnt lgkmcnt(0)
	s_barrier
	global_load_lds_dwordx4 v[80:81], off nt
	v_lshl_add_u64 v[80:81], s[0:1], 0, v[74:75]
	s_mov_b32 m0, s2
	v_readfirstlane_b32 s2, v1
	v_add_u32_e32 v1, s17, v119
	global_load_lds_dwordx4 v[80:81], off nt
	v_lshl_add_u64 v[80:81], s[0:1], 0, v[124:125]
	s_mov_b32 m0, s2
	v_readfirstlane_b32 s2, v1
	global_load_lds_dwordx4 v[80:81], off nt
	v_lshl_add_u64 v[80:81], s[0:1], 0, v[126:127]
	s_mov_b32 m0, s2
	v_accvgpr_write_b32 a53, v33
	v_accvgpr_write_b32 a2, v62
	v_accvgpr_write_b32 a7, v5
	v_accvgpr_write_b32 a22, v124
	v_accvgpr_write_b32 a30, v126
	global_load_lds_dwordx4 v[80:81], off nt
	v_accvgpr_write_b32 a52, v32
	v_accvgpr_write_b32 a3, v63
	v_accvgpr_write_b32 a6, v4
	v_mov_b64_e32 v[32:33], v[72:73]
	v_accvgpr_write_b32 a23, v125
	v_accvgpr_write_b32 a31, v127
	v_add_u32_e32 v2, 0x1d010, v122
	v_accvgpr_write_b32 a10, v122
	v_add_u32_e32 v5, 0x1d000, v60
	v_mov_b32_e32 v4, v60
	ds_read_b64 v[62:63], v2
	ds_read_b64 v[60:61], v2 offset:288
	ds_read_b64 v[72:73], v2 offset:576
	ds_read_b64 v[70:71], v2 offset:1728
	ds_read_b64 v[68:69], v2 offset:2016
	ds_read_b64 v[82:83], v2 offset:2304
	ds_read_b64 v[80:81], v2 offset:3456
	ds_read_b64 v[84:85], v2 offset:3744
	ds_read_b64 v[126:127], v2 offset:4032
	ds_read_b64 v[124:125], v2 offset:5184
	ds_read_b64 v[122:123], v2 offset:5472
	ds_read_b64 v[120:121], v2 offset:5760
	ds_read_b32 v43, v5
	ds_read_b32 v19, v5 offset:288
	ds_read_b32 v39, v5 offset:576
	ds_read_b32 v25, v5 offset:1728
	ds_read_b32 v7, v5 offset:2016
	ds_read_b32 v21, v5 offset:2304
	ds_read_b32 v11, v5 offset:3456
	ds_read_b32 v35, v5 offset:3744
	ds_read_b32 v59, v5 offset:4032
	ds_read_b32 v57, v5 offset:5184
	ds_read_b32 v51, v5 offset:5472
	ds_read_b32 v49, v5 offset:5760
	s_waitcnt lgkmcnt(0)
	v_mov_b64_e32 v[100:101], v[86:87]
	v_mov_b32_e32 v46, v43
	v_mov_b32_e32 v113, v63
	v_mov_b32_e32 v26, v19
	v_mov_b32_dpp v46, v63 row_shr:1 row_mask:0xf bank_mask:0xf
	v_pk_mul_f32 v[88:89], v[112:113], v[46:47]
	v_mov_b32_dpp v43, v62 row_shl:1 row_mask:0xf bank_mask:0xf
	v_pk_fma_f32 v[88:89], v[62:63], v[116:117], v[88:89] op_sel_hi:[0,1,1]
	v_pk_mov_b32 v[62:63], v[62:63], v[100:101] op_sel:[1,0]
	v_mov_b32_dpp v26, v61 row_shr:1 row_mask:0xf bank_mask:0xf
	v_mov_b32_e32 v17, v61
	v_pk_fma_f32 v[62:63], v[62:63], v[42:43], v[88:89]
	v_pk_mul_f32 v[88:89], v[16:17], v[26:27]
	v_accvgpr_write_b32 a34, v16
	v_accvgpr_read_b32 v16, a52
	v_accvgpr_read_b32 v17, a53
	v_mov_b32_dpp v19, v60 row_shl:1 row_mask:0xf bank_mask:0xf
	v_pk_fma_f32 v[88:89], v[60:61], v[114:115], v[88:89] op_sel_hi:[0,1,1]
	v_pk_mov_b32 v[60:61], v[60:61], v[16:17] op_sel:[1,0]
	v_mov_b32_e32 v44, v39
	v_accvgpr_write_b32 a28, v14
	v_pk_fma_f32 v[60:61], v[60:61], v[18:19], v[88:89]
	v_pk_add_f32 v[62:63], v[62:63], 0 op_sel_hi:[1,0]
	v_mov_b32_dpp v44, v73 row_shr:1 row_mask:0xf bank_mask:0xf
	v_mov_b32_e32 v1, v73
	v_accvgpr_read_b32 v14, a44
	v_accvgpr_read_b32 v89, a21
	v_pk_add_f32 v[60:61], v[62:63], v[60:61]
	v_pk_mul_f32 v[62:63], v[0:1], v[44:45]
	v_accvgpr_read_b32 v15, a45
	v_accvgpr_read_b32 v88, a20
	v_mov_b32_dpp v39, v72 row_shl:1 row_mask:0xf bank_mask:0xf
	v_pk_fma_f32 v[62:63], v[72:73], v[14:15], v[62:63] op_sel_hi:[0,1,1]
	v_pk_mov_b32 v[72:73], v[72:73], v[88:89] op_sel:[1,0]
	v_mov_b32_e32 v36, v25
	v_pk_fma_f32 v[62:63], v[72:73], v[38:39], v[62:63]
	s_mov_b64 s[0:1], 0x400000
	v_pk_add_f32 v[60:61], v[60:61], v[62:63]
	v_mov_b32_dpp v36, v71 row_shr:1 row_mask:0xf bank_mask:0xf
	v_mov_b32_e32 v65, v71
	v_accvgpr_read_b32 v87, a41
	v_lshl_add_u64 v[62:63], v[54:55], 0, s[0:1]
	v_mov_b32_e32 v128, v60
	v_mov_b32_e32 v129, v61
	v_pk_mul_f32 v[60:61], v[64:65], v[36:37]
	v_accvgpr_read_b32 v86, a40
	v_mov_b32_e32 v12, v7
	v_mov_b32_dpp v25, v70 row_shl:1 row_mask:0xf bank_mask:0xf
	v_pk_fma_f32 v[60:61], v[70:71], v[86:87], v[60:61] op_sel_hi:[0,1,1]
	v_mov_b32_e32 v62, v71
	v_mov_b32_e32 v63, v101
	v_mov_b32_dpp v12, v69 row_shr:1 row_mask:0xf bank_mask:0xf
	v_mov_b32_e32 v29, v69
	v_accvgpr_read_b32 v107, a37
	v_pk_fma_f32 v[60:61], v[62:63], v[24:25], v[60:61]
	v_pk_mul_f32 v[62:63], v[28:29], v[12:13]
	v_accvgpr_read_b32 v106, a36
	v_mov_b32_dpp v7, v68 row_shl:1 row_mask:0xf bank_mask:0xf
	v_pk_fma_f32 v[62:63], v[68:69], v[106:107], v[62:63] op_sel_hi:[0,1,1]
	v_mov_b32_e32 v68, v69
	v_mov_b32_e32 v69, v17
	v_mov_b32_e32 v78, v21
	v_pk_fma_f32 v[62:63], v[68:69], v[6:7], v[62:63]
	v_pk_add_f32 v[60:61], v[60:61], 0 op_sel_hi:[1,0]
	v_mov_b32_dpp v78, v83 row_shr:1 row_mask:0xf bank_mask:0xf
	v_mov_b32_e32 v53, v83
	v_accvgpr_read_b32 v14, a24
	v_pk_add_f32 v[60:61], v[60:61], v[62:63]
	v_pk_mul_f32 v[62:63], v[52:53], v[78:79]
	v_accvgpr_read_b32 v15, a25
	v_mov_b32_dpp v21, v82 row_shl:1 row_mask:0xf bank_mask:0xf
	v_pk_fma_f32 v[62:63], v[82:83], v[14:15], v[62:63] op_sel_hi:[0,1,1]
	v_mov_b32_e32 v68, v83
	v_mov_b32_e32 v69, v89
	v_pk_fma_f32 v[62:63], v[68:69], v[20:21], v[62:63]
	v_mov_b32_e32 v76, v11
	v_pk_add_f32 v[60:61], v[60:61], v[62:63]
	s_mov_b64 s[0:1], 0x410000
	v_mov_b32_dpp v76, v81 row_shr:1 row_mask:0xf bank_mask:0xf
	v_mov_b32_e32 v41, v81
	v_lshl_add_u64 v[136:137], v[134:135], 0, s[0:1]
	s_nop 1
	s_mov_b64 vcc, s[28:29]
	s_nop 0
	v_cndmask_b32_dpp v130, v60, v128, vcc quad_perm:[1,0,3,2] row_mask:0xf bank_mask:0xf
	v_cndmask_b32_dpp v131, v61, v129, vcc quad_perm:[1,0,3,2] row_mask:0xf bank_mask:0xf
	s_mov_b64 vcc, s[30:31]
	s_nop 0
	v_cndmask_b32_dpp v132, v128, v60, vcc quad_perm:[1,0,3,2] row_mask:0xf bank_mask:0xf
	v_cndmask_b32_dpp v133, v129, v61, vcc quad_perm:[1,0,3,2] row_mask:0xf bank_mask:0xf
	global_store_dwordx4 v[136:137], v[130:133], off sc0 sc1 nt
	s_nop 1
	v_pk_mul_f32 v[60:61], v[40:41], v[76:77]
	v_accvgpr_write_b32 a36, v66
	v_pk_fma_f32 v[60:61], v[80:81], v[66:67], v[60:61] op_sel_hi:[0,1,1]
	v_accvgpr_write_b32 a37, v67
	v_accvgpr_read_b32 v67, a29
	v_accvgpr_write_b32 a5, v2
	v_accvgpr_write_b32 a38, v100
	v_accvgpr_read_b32 v66, a28
	v_mov_b32_e32 v2, v35
	v_accvgpr_write_b32 a39, v101
	v_mov_b32_dpp v11, v80 row_shl:1 row_mask:0xf bank_mask:0xf
	v_pk_mov_b32 v[62:63], v[80:81], v[66:67] op_sel:[1,0]
	v_mov_b32_dpp v2, v85 row_shr:1 row_mask:0xf bank_mask:0xf
	v_mov_b32_e32 v23, v85
	v_accvgpr_read_b32 v101, a33
	v_pk_fma_f32 v[60:61], v[62:63], v[10:11], v[60:61]
	v_pk_mul_f32 v[62:63], v[22:23], v[2:3]
	v_accvgpr_read_b32 v100, a32
	v_mov_b32_dpp v35, v84 row_shl:1 row_mask:0xf bank_mask:0xf
	v_pk_fma_f32 v[62:63], v[84:85], v[100:101], v[62:63] op_sel_hi:[0,1,1]
	v_pk_mov_b32 v[68:69], v[84:85], v[8:9] op_sel:[1,0]
	v_mov_b32_e32 v92, v59
	v_pk_fma_f32 v[62:63], v[68:69], v[34:35], v[62:63]
	v_pk_add_f32 v[60:61], v[60:61], 0 op_sel_hi:[1,0]
	v_mov_b32_dpp v92, v127 row_shr:1 row_mask:0xf bank_mask:0xf
	v_mov_b32_e32 v97, v127
	v_accvgpr_read_b32 v17, a9
	v_accvgpr_read_b32 v71, a49
	v_pk_add_f32 v[60:61], v[60:61], v[62:63]
	v_pk_mul_f32 v[62:63], v[96:97], v[92:93]
	v_accvgpr_read_b32 v16, a8
	v_accvgpr_read_b32 v70, a48
	v_mov_b32_dpp v59, v126 row_shl:1 row_mask:0xf bank_mask:0xf
	v_pk_fma_f32 v[62:63], v[126:127], v[16:17], v[62:63] op_sel_hi:[0,1,1]
	v_pk_mov_b32 v[68:69], v[126:127], v[70:71] op_sel:[1,0]
	v_mov_b32_e32 v94, v57
	v_pk_fma_f32 v[62:63], v[68:69], v[58:59], v[62:63]
	v_accvgpr_write_b32 a20, v28
	v_pk_add_f32 v[60:61], v[60:61], v[62:63]
	s_mov_b64 s[0:1], 0x420000
	v_mov_b32_dpp v94, v125 row_shr:1 row_mask:0xf bank_mask:0xf
	v_mov_b32_e32 v99, v125
	v_accvgpr_read_b32 v29, a3
	v_lshl_add_u64 v[62:63], v[54:55], 0, s[0:1]
	v_mov_b32_e32 v128, v60
	v_mov_b32_e32 v129, v61
	v_pk_mul_f32 v[60:61], v[98:99], v[94:95]
	v_accvgpr_read_b32 v28, a2
	v_mov_b32_e32 v102, v51
	v_mov_b32_dpp v57, v124 row_shl:1 row_mask:0xf bank_mask:0xf
	v_pk_fma_f32 v[60:61], v[124:125], v[28:29], v[60:61] op_sel_hi:[0,1,1]
	v_mov_b32_e32 v62, v125
	v_mov_b32_e32 v63, v67
	v_mov_b32_dpp v102, v123 row_shr:1 row_mask:0xf bank_mask:0xf
	v_mov_b32_e32 v105, v123
	v_pk_fma_f32 v[60:61], v[62:63], v[56:57], v[60:61]
	v_pk_mul_f32 v[62:63], v[104:105], v[102:103]
	v_mov_b32_dpp v51, v122 row_shl:1 row_mask:0xf bank_mask:0xf
	v_pk_fma_f32 v[62:63], v[122:123], v[30:31], v[62:63] op_sel_hi:[0,1,1]
	v_accvgpr_write_b32 a28, v30
	v_mov_b32_e32 v68, v123
	v_mov_b32_e32 v69, v9
	v_mov_b32_e32 v108, v49
	v_accvgpr_write_b32 a29, v31
	v_pk_fma_f32 v[62:63], v[68:69], v[50:51], v[62:63]
	v_pk_add_f32 v[60:61], v[60:61], 0 op_sel_hi:[1,0]
	v_mov_b32_dpp v108, v121 row_shr:1 row_mask:0xf bank_mask:0xf
	v_mov_b32_e32 v111, v121
	v_accvgpr_read_b32 v31, a7
	v_pk_add_f32 v[60:61], v[60:61], v[62:63]
	v_pk_mul_f32 v[62:63], v[110:111], v[108:109]
	v_accvgpr_read_b32 v30, a6
	v_mov_b32_dpp v49, v120 row_shl:1 row_mask:0xf bank_mask:0xf
	v_pk_fma_f32 v[62:63], v[120:121], v[30:31], v[62:63] op_sel_hi:[0,1,1]
	v_mov_b32_e32 v68, v121
	v_mov_b32_e32 v69, v71
	v_pk_fma_f32 v[62:63], v[68:69], v[48:49], v[62:63]
	s_mov_b64 s[0:1], 0x430000
	v_pk_add_f32 v[60:61], v[60:61], v[62:63]
	v_lshl_add_u64 v[136:137], v[134:135], 0, s[0:1]
	v_add_u32_e32 v1, s16, v118
	s_add_u32 s0, s10, 0x1800000
	v_accvgpr_write_b32 a26, v114
	s_nop 1
	s_mov_b64 vcc, s[28:29]
	s_nop 0
	v_cndmask_b32_dpp v130, v60, v128, vcc quad_perm:[1,0,3,2] row_mask:0xf bank_mask:0xf
	v_cndmask_b32_dpp v131, v61, v129, vcc quad_perm:[1,0,3,2] row_mask:0xf bank_mask:0xf
	s_mov_b64 vcc, s[30:31]
	s_nop 0
	v_cndmask_b32_dpp v132, v128, v60, vcc quad_perm:[1,0,3,2] row_mask:0xf bank_mask:0xf
	v_cndmask_b32_dpp v133, v129, v61, vcc quad_perm:[1,0,3,2] row_mask:0xf bank_mask:0xf
	global_store_dwordx4 v[136:137], v[130:133], off sc0 sc1 nt
	s_nop 1
	v_readfirstlane_b32 s2, v1
	s_addc_u32 s1, s11, 0
	v_add_u32_e32 v1, s16, v90
	v_accvgpr_write_b32 a18, v116
	v_accvgpr_write_b32 a27, v115
	s_waitcnt vmcnt(16)
	v_lshl_add_u64 v[60:61], s[0:1], 0, v[32:33]
	s_mov_b32 m0, s2
	v_readfirstlane_b32 s2, v1
	v_add_u32_e32 v1, s16, v91
	v_accvgpr_read_b32 v115, a23
	v_accvgpr_write_b32 a19, v117
	s_waitcnt lgkmcnt(0)
	s_barrier
	global_load_lds_dwordx4 v[60:61], off nt
	v_lshl_add_u64 v[60:61], s[0:1], 0, v[74:75]
	s_mov_b32 m0, s2
	v_readfirstlane_b32 s2, v1
	v_accvgpr_read_b32 v114, a22
	v_add_u32_e32 v1, s16, v119
	v_accvgpr_read_b32 v117, a31
	global_load_lds_dwordx4 v[60:61], off nt
	v_lshl_add_u64 v[60:61], s[0:1], 0, v[114:115]
	s_mov_b32 m0, s2
	v_readfirstlane_b32 s2, v1
	v_accvgpr_read_b32 v116, a30
	global_load_lds_dwordx4 v[60:61], off nt
	v_lshl_add_u64 v[60:61], s[0:1], 0, v[116:117]
	s_mov_b32 m0, s2
	v_accvgpr_write_b32 a1, v5
	global_load_lds_dwordx4 v[60:61], off nt
	v_accvgpr_read_b32 v5, a10
	v_add_u32_e32 v2, 16, v5
	ds_read_b64 v[60:61], v2
	ds_read_b64 v[62:63], v2 offset:288
	ds_read_b64 v[68:69], v2 offset:576
	ds_read_b64 v[70:71], v2 offset:1728
	ds_read_b64 v[72:73], v2 offset:2016
	ds_read_b64 v[82:83], v2 offset:2304
	ds_read_b64 v[80:81], v2 offset:3456
	ds_read_b64 v[84:85], v2 offset:3744
	ds_read_b64 v[124:125], v2 offset:4032
	ds_read_b64 v[122:123], v2 offset:5184
	ds_read_b64 v[120:121], v2 offset:5472
	ds_read_b64 v[90:91], v2 offset:5760
	ds_read_b32 v43, v4
	ds_read_b32 v19, v4 offset:288
	ds_read_b32 v39, v4 offset:576
	ds_read_b32 v25, v4 offset:1728
	ds_read_b32 v7, v4 offset:2016
	ds_read_b32 v21, v4 offset:2304
	ds_read_b32 v11, v4 offset:3456
	ds_read_b32 v35, v4 offset:3744
	ds_read_b32 v59, v4 offset:4032
	ds_read_b32 v57, v4 offset:5184
	ds_read_b32 v51, v4 offset:5472
	ds_read_b32 v49, v4 offset:5760
	s_waitcnt lgkmcnt(0)
	v_accvgpr_write_b32 a46, v88
	v_mov_b32_e32 v46, v43
	v_accvgpr_write_b32 a8, v8
	v_mov_b32_e32 v113, v61
	v_mov_b32_dpp v46, v61 row_shr:1 row_mask:0xf bank_mask:0xf
	v_accvgpr_mov_b32 a42, a52
	v_accvgpr_write_b32 a47, v89
	v_accvgpr_write_b32 a9, v9
	v_pk_mul_f32 v[88:89], v[112:113], v[46:47]
	v_accvgpr_write_b32 a40, v112
	v_accvgpr_read_b32 v8, a18
	v_accvgpr_read_b32 v113, a39
	v_accvgpr_mov_b32 a43, a53
	v_accvgpr_write_b32 a51, v33
	v_accvgpr_write_b32 a52, v74
	v_accvgpr_read_b32 v9, a19
	v_accvgpr_read_b32 v112, a38
	v_mov_b32_e32 v26, v19
	v_accvgpr_write_b32 a50, v32
	v_accvgpr_write_b32 a53, v75
	v_mov_b32_dpp v43, v60 row_shl:1 row_mask:0xf bank_mask:0xf
	v_pk_fma_f32 v[88:89], v[60:61], v[8:9], v[88:89] op_sel_hi:[0,1,1]
	v_pk_mov_b32 v[60:61], v[60:61], v[112:113] op_sel:[1,0]
	v_mov_b32_dpp v26, v63 row_shr:1 row_mask:0xf bank_mask:0xf
	v_accvgpr_read_b32 v32, a34
	v_mov_b32_e32 v33, v63
	v_accvgpr_read_b32 v127, a27
	v_accvgpr_read_b32 v75, a43
	v_pk_fma_f32 v[60:61], v[60:61], v[42:43], v[88:89]
	v_pk_mul_f32 v[88:89], v[32:33], v[26:27]
	v_accvgpr_read_b32 v126, a26
	v_accvgpr_read_b32 v74, a42
	v_mov_b32_dpp v19, v62 row_shl:1 row_mask:0xf bank_mask:0xf
	v_pk_fma_f32 v[88:89], v[62:63], v[126:127], v[88:89] op_sel_hi:[0,1,1]
	v_pk_mov_b32 v[62:63], v[62:63], v[74:75] op_sel:[1,0]
	v_mov_b32_e32 v44, v39
	v_accvgpr_mov_b32 a14, a48
	v_pk_fma_f32 v[62:63], v[62:63], v[18:19], v[88:89]
	v_pk_add_f32 v[60:61], v[60:61], 0 op_sel_hi:[1,0]
	v_mov_b32_dpp v44, v69 row_shr:1 row_mask:0xf bank_mask:0xf
	v_mov_b32_e32 v1, v69
	v_accvgpr_mov_b32 a15, a49
	v_pk_add_f32 v[60:61], v[60:61], v[62:63]
	v_pk_mul_f32 v[62:63], v[0:1], v[44:45]
	v_accvgpr_write_b32 a48, v0
	v_accvgpr_read_b32 v89, a45
	v_accvgpr_read_b32 v0, a46
	v_accvgpr_read_b32 v88, a44
	v_accvgpr_read_b32 v1, a47
	v_mov_b32_dpp v39, v68 row_shl:1 row_mask:0xf bank_mask:0xf
	v_pk_fma_f32 v[62:63], v[68:69], v[88:89], v[62:63] op_sel_hi:[0,1,1]
	v_pk_mov_b32 v[68:69], v[68:69], v[0:1] op_sel:[1,0]
	v_mov_b32_e32 v36, v25
	v_pk_fma_f32 v[62:63], v[68:69], v[38:39], v[62:63]
	s_mov_b64 s[0:1], 0x800000
	v_pk_add_f32 v[60:61], v[60:61], v[62:63]
	v_mov_b32_dpp v36, v71 row_shr:1 row_mask:0xf bank_mask:0xf
	v_mov_b32_e32 v65, v71
	v_lshl_add_u64 v[62:63], v[54:55], 0, s[0:1]
	v_mov_b32_e32 v128, v60
	v_mov_b32_e32 v129, v61
	v_pk_mul_f32 v[60:61], v[64:65], v[36:37]
	v_mov_b64_e32 v[118:119], v[86:87]
	v_mov_b32_e32 v12, v7
	v_accvgpr_write_b32 a24, v32
	v_mov_b32_dpp v25, v70 row_shl:1 row_mask:0xf bank_mask:0xf
	v_pk_fma_f32 v[60:61], v[70:71], v[118:119], v[60:61] op_sel_hi:[0,1,1]
	v_mov_b32_e32 v62, v71
	v_mov_b32_e32 v63, v113
	v_mov_b32_dpp v12, v73 row_shr:1 row_mask:0xf bank_mask:0xf
	v_accvgpr_read_b32 v32, a20
	v_mov_b32_e32 v33, v73
	v_pk_fma_f32 v[60:61], v[62:63], v[24:25], v[60:61]
	v_pk_mul_f32 v[62:63], v[32:33], v[12:13]
	v_mov_b32_dpp v7, v72 row_shl:1 row_mask:0xf bank_mask:0xf
	v_pk_fma_f32 v[62:63], v[72:73], v[106:107], v[62:63] op_sel_hi:[0,1,1]
	v_mov_b32_e32 v68, v73
	v_mov_b32_e32 v69, v75
	v_mov_b32_e32 v78, v21
	v_pk_fma_f32 v[62:63], v[68:69], v[6:7], v[62:63]
	v_pk_add_f32 v[60:61], v[60:61], 0 op_sel_hi:[1,0]
	v_mov_b32_dpp v78, v83 row_shr:1 row_mask:0xf bank_mask:0xf
	v_mov_b32_e32 v53, v83
	v_pk_add_f32 v[60:61], v[60:61], v[62:63]
	v_pk_mul_f32 v[62:63], v[52:53], v[78:79]
	v_mov_b32_dpp v21, v82 row_shl:1 row_mask:0xf bank_mask:0xf
	v_pk_fma_f32 v[62:63], v[82:83], v[14:15], v[62:63] op_sel_hi:[0,1,1]
	v_mov_b32_e32 v68, v83
	v_mov_b32_e32 v69, v1
	v_accvgpr_write_b32 a19, v15
	v_pk_fma_f32 v[62:63], v[68:69], v[20:21], v[62:63]
	v_mov_b32_e32 v76, v11
	v_accvgpr_write_b32 a18, v14
	v_pk_add_f32 v[60:61], v[60:61], v[62:63]
	s_mov_b64 s[0:1], 0x810000
	v_mov_b32_dpp v76, v81 row_shr:1 row_mask:0xf bank_mask:0xf
	v_mov_b32_e32 v41, v81
	v_accvgpr_read_b32 v14, a36
	v_accvgpr_write_b32 a6, v2
	v_lshl_add_u64 v[136:137], v[134:135], 0, s[0:1]
	s_nop 1
	s_mov_b64 vcc, s[28:29]
	s_nop 0
	v_cndmask_b32_dpp v130, v60, v128, vcc quad_perm:[1,0,3,2] row_mask:0xf bank_mask:0xf
	v_cndmask_b32_dpp v131, v61, v129, vcc quad_perm:[1,0,3,2] row_mask:0xf bank_mask:0xf
	s_mov_b64 vcc, s[30:31]
	s_nop 0
	v_cndmask_b32_dpp v132, v128, v60, vcc quad_perm:[1,0,3,2] row_mask:0xf bank_mask:0xf
	v_cndmask_b32_dpp v133, v129, v61, vcc quad_perm:[1,0,3,2] row_mask:0xf bank_mask:0xf
	global_store_dwordx4 v[136:137], v[130:133], off sc0 sc1 nt
	s_nop 1
	v_pk_mul_f32 v[60:61], v[40:41], v[76:77]
	v_accvgpr_read_b32 v15, a37
	v_mov_b32_e32 v2, v35
	v_mov_b32_dpp v11, v80 row_shl:1 row_mask:0xf bank_mask:0xf
	v_pk_fma_f32 v[60:61], v[80:81], v[14:15], v[60:61] op_sel_hi:[0,1,1]
	v_pk_mov_b32 v[62:63], v[80:81], v[66:67] op_sel:[1,0]
	v_mov_b32_dpp v2, v85 row_shr:1 row_mask:0xf bank_mask:0xf
	v_mov_b32_e32 v23, v85
	v_accvgpr_read_b32 v15, a9
	v_pk_fma_f32 v[60:61], v[62:63], v[10:11], v[60:61]
	v_pk_mul_f32 v[62:63], v[22:23], v[2:3]
	v_accvgpr_read_b32 v14, a8
	v_mov_b32_dpp v35, v84 row_shl:1 row_mask:0xf bank_mask:0xf
	v_pk_fma_f32 v[62:63], v[84:85], v[100:101], v[62:63] op_sel_hi:[0,1,1]
	v_pk_mov_b32 v[68:69], v[84:85], v[14:15] op_sel:[1,0]
	v_mov_b32_e32 v92, v59
	v_pk_fma_f32 v[62:63], v[68:69], v[34:35], v[62:63]
	v_pk_add_f32 v[60:61], v[60:61], 0 op_sel_hi:[1,0]
	v_mov_b32_dpp v92, v125 row_shr:1 row_mask:0xf bank_mask:0xf
	v_mov_b32_e32 v97, v125
	v_accvgpr_read_b32 v71, a15
	v_pk_add_f32 v[60:61], v[60:61], v[62:63]
	v_pk_mul_f32 v[62:63], v[96:97], v[92:93]
	v_accvgpr_read_b32 v70, a14
	v_mov_b32_dpp v59, v124 row_shl:1 row_mask:0xf bank_mask:0xf
	v_pk_fma_f32 v[62:63], v[124:125], v[16:17], v[62:63] op_sel_hi:[0,1,1]
	v_pk_mov_b32 v[68:69], v[124:125], v[70:71] op_sel:[1,0]
	v_mov_b32_e32 v94, v57
	v_pk_fma_f32 v[62:63], v[68:69], v[58:59], v[62:63]
	s_mov_b64 s[0:1], 0x820000
	v_pk_add_f32 v[60:61], v[60:61], v[62:63]
	v_mov_b32_dpp v94, v123 row_shr:1 row_mask:0xf bank_mask:0xf
	v_mov_b32_e32 v99, v123
	v_accvgpr_write_b32 a31, v17
	v_lshl_add_u64 v[62:63], v[54:55], 0, s[0:1]
	v_mov_b32_e32 v128, v60
	v_mov_b32_e32 v129, v61
	v_pk_mul_f32 v[60:61], v[98:99], v[94:95]
	v_mov_b32_e32 v102, v51
	v_accvgpr_write_b32 a30, v16
	v_mov_b32_dpp v57, v122 row_shl:1 row_mask:0xf bank_mask:0xf
	v_pk_fma_f32 v[60:61], v[122:123], v[28:29], v[60:61] op_sel_hi:[0,1,1]
	v_mov_b32_e32 v62, v123
	v_mov_b32_e32 v63, v67
	v_mov_b32_dpp v102, v121 row_shr:1 row_mask:0xf bank_mask:0xf
	v_mov_b32_e32 v105, v121
	v_accvgpr_read_b32 v16, a28
	v_pk_fma_f32 v[60:61], v[62:63], v[56:57], v[60:61]
	v_pk_mul_f32 v[62:63], v[104:105], v[102:103]
	v_accvgpr_read_b32 v17, a29
	v_mov_b32_dpp v51, v120 row_shl:1 row_mask:0xf bank_mask:0xf
	v_pk_fma_f32 v[62:63], v[120:121], v[16:17], v[62:63] op_sel_hi:[0,1,1]
	v_mov_b32_e32 v68, v121
	v_mov_b32_e32 v69, v15
	v_mov_b32_e32 v108, v49
	v_pk_fma_f32 v[62:63], v[68:69], v[50:51], v[62:63]
	v_pk_add_f32 v[60:61], v[60:61], 0 op_sel_hi:[1,0]
	v_mov_b32_dpp v108, v91 row_shr:1 row_mask:0xf bank_mask:0xf
	v_mov_b32_e32 v111, v91
	v_pk_add_f32 v[60:61], v[60:61], v[62:63]
	v_pk_mul_f32 v[62:63], v[110:111], v[108:109]
	v_mov_b32_dpp v49, v90 row_shl:1 row_mask:0xf bank_mask:0xf
	v_pk_fma_f32 v[62:63], v[90:91], v[30:31], v[62:63] op_sel_hi:[0,1,1]
	v_mov_b32_e32 v68, v91
	v_mov_b32_e32 v69, v71
	v_pk_fma_f32 v[62:63], v[68:69], v[48:49], v[62:63]
	s_mov_b64 s[0:1], 0x830000
	v_mov_b32_e32 v0, v22
	v_pk_add_f32 v[60:61], v[60:61], v[62:63]
	v_lshl_add_u64 v[136:137], v[134:135], 0, s[0:1]
	s_add_u32 s0, s10, 0x1c00000
	v_accvgpr_read_b32 v22, a50
	v_accvgpr_read_b32 v1, a72
	s_addc_u32 s1, s11, 0
	v_accvgpr_read_b32 v23, a51
	s_nop 1
	s_mov_b64 vcc, s[28:29]
	s_nop 0
	v_cndmask_b32_dpp v130, v60, v128, vcc quad_perm:[1,0,3,2] row_mask:0xf bank_mask:0xf
	v_cndmask_b32_dpp v131, v61, v129, vcc quad_perm:[1,0,3,2] row_mask:0xf bank_mask:0xf
	s_mov_b64 vcc, s[30:31]
	s_nop 0
	v_cndmask_b32_dpp v132, v128, v60, vcc quad_perm:[1,0,3,2] row_mask:0xf bank_mask:0xf
	v_cndmask_b32_dpp v133, v129, v61, vcc quad_perm:[1,0,3,2] row_mask:0xf bank_mask:0xf
	global_store_dwordx4 v[136:137], v[130:133], off sc0 sc1 nt
	s_nop 1
	v_readfirstlane_b32 s2, v1
	v_lshl_add_u64 v[60:61], s[0:1], 0, v[22:23]
	v_accvgpr_read_b32 v1, a12
	v_accvgpr_read_b32 v22, a52
	s_waitcnt vmcnt(18)
	s_mov_b32 m0, s2
	v_readfirstlane_b32 s2, v1
	v_accvgpr_read_b32 v23, a53
	v_accvgpr_read_b32 v1, a13
	s_waitcnt lgkmcnt(0)
	s_barrier
	global_load_lds_dwordx4 v[60:61], off nt
	v_lshl_add_u64 v[60:61], s[0:1], 0, v[22:23]
	s_mov_b32 m0, s2
	v_readfirstlane_b32 s2, v1
	v_accvgpr_read_b32 v1, a16
	global_load_lds_dwordx4 v[60:61], off nt
	v_lshl_add_u64 v[60:61], s[0:1], 0, v[114:115]
	s_mov_b32 m0, s2
	v_readfirstlane_b32 s2, v1
	global_load_lds_dwordx4 v[60:61], off nt
	v_lshl_add_u64 v[60:61], s[0:1], 0, v[116:117]
	s_mov_b32 m0, s2
	v_accvgpr_write_b32 a22, v30
	v_accvgpr_write_b32 a44, v70
	global_load_lds_dwordx4 v[60:61], off nt
	v_accvgpr_write_b32 a2, v106
	v_accvgpr_write_b32 a34, v74
	v_accvgpr_write_b32 a23, v31
	v_accvgpr_write_b32 a45, v71
	v_add_u32_e32 v2, 0x7010, v5
	v_mov_b32_e32 v31, v5
	v_add_u32_e32 v5, 0x7000, v4
	ds_read_b64 v[60:61], v2
	ds_read_b64 v[62:63], v2 offset:288
	ds_read_b64 v[68:69], v2 offset:576
	ds_read_b64 v[70:71], v2 offset:1728
	ds_read_b64 v[72:73], v2 offset:2016
	ds_read_b64 v[82:83], v2 offset:2304
	ds_read_b64 v[80:81], v2 offset:3456
	ds_read_b64 v[84:85], v2 offset:3744
	ds_read_b64 v[116:117], v2 offset:4032
	ds_read_b64 v[114:115], v2 offset:5184
	ds_read_b64 v[112:113], v2 offset:5472
	ds_read_b64 v[90:91], v2 offset:5760
	ds_read_b32 v43, v5
	ds_read_b32 v19, v5 offset:288
	ds_read_b32 v39, v5 offset:576
	ds_read_b32 v25, v5 offset:1728
	ds_read_b32 v7, v5 offset:2016
	ds_read_b32 v21, v5 offset:2304
	ds_read_b32 v11, v5 offset:3456
	ds_read_b32 v35, v5 offset:3744
	ds_read_b32 v59, v5 offset:4032
	ds_read_b32 v57, v5 offset:5184
	ds_read_b32 v51, v5 offset:5472
	ds_read_b32 v49, v5 offset:5760
	s_waitcnt lgkmcnt(0)
	v_accvgpr_write_b32 a3, v107
	v_mov_b32_e32 v46, v43
	v_accvgpr_write_b32 a35, v75
	v_accvgpr_read_b32 v74, a40
	v_mov_b32_dpp v46, v61 row_shr:1 row_mask:0xf bank_mask:0xf
	v_mov_b32_e32 v75, v61
	v_accvgpr_read_b32 v107, a39
	v_accvgpr_write_b32 a10, v100
	v_pk_mul_f32 v[86:87], v[74:75], v[46:47]
	v_accvgpr_read_b32 v106, a38
	v_mov_b32_e32 v26, v19
	v_accvgpr_write_b32 a11, v101
	v_mov_b32_dpp v43, v60 row_shl:1 row_mask:0xf bank_mask:0xf
	v_mov_b32_e32 v32, v74
	v_pk_fma_f32 v[86:87], v[60:61], v[8:9], v[86:87] op_sel_hi:[0,1,1]
	v_pk_mov_b32 v[60:61], v[60:61], v[106:107] op_sel:[1,0]
	v_mov_b32_dpp v26, v63 row_shr:1 row_mask:0xf bank_mask:0xf
	v_accvgpr_read_b32 v74, a24
	v_mov_b32_e32 v75, v63
	v_accvgpr_read_b32 v101, a35
	v_pk_fma_f32 v[60:61], v[60:61], v[42:43], v[86:87]
	v_pk_mul_f32 v[86:87], v[74:75], v[26:27]
	v_accvgpr_read_b32 v100, a34
	v_accvgpr_write_b32 a14, v66
	v_mov_b32_dpp v19, v62 row_shl:1 row_mask:0xf bank_mask:0xf
	v_pk_fma_f32 v[86:87], v[62:63], v[126:127], v[86:87] op_sel_hi:[0,1,1]
	v_pk_mov_b32 v[62:63], v[62:63], v[100:101] op_sel:[1,0]
	v_mov_b32_e32 v44, v39
	v_accvgpr_write_b32 a42, v64
	v_accvgpr_write_b32 a15, v67
	v_mov_b32_e32 v66, v4
	v_pk_fma_f32 v[62:63], v[62:63], v[18:19], v[86:87]
	v_pk_add_f32 v[60:61], v[60:61], 0 op_sel_hi:[1,0]
	v_mov_b32_dpp v44, v69 row_shr:1 row_mask:0xf bank_mask:0xf
	v_accvgpr_read_b32 v64, a48
	v_mov_b32_e32 v65, v69
	v_accvgpr_read_b32 v4, a46
	v_pk_add_f32 v[60:61], v[60:61], v[62:63]
	v_pk_mul_f32 v[62:63], v[64:65], v[44:45]
	v_accvgpr_read_b32 v5, a47
	v_mov_b32_dpp v39, v68 row_shl:1 row_mask:0xf bank_mask:0xf
	v_pk_fma_f32 v[62:63], v[68:69], v[88:89], v[62:63] op_sel_hi:[0,1,1]
	v_pk_mov_b32 v[68:69], v[68:69], v[4:5] op_sel:[1,0]
	v_mov_b32_e32 v36, v25
	v_pk_fma_f32 v[62:63], v[68:69], v[38:39], v[62:63]
	s_mov_b64 s[0:1], 0xc00000
	v_pk_add_f32 v[60:61], v[60:61], v[62:63]
	v_mov_b32_dpp v36, v71 row_shr:1 row_mask:0xf bank_mask:0xf
	v_accvgpr_read_b32 v22, a42
	v_mov_b32_e32 v23, v71
	v_accvgpr_mov_b32 a26, a20
	v_accvgpr_write_b32 a20, v28
	v_lshl_add_u64 v[62:63], v[54:55], 0, s[0:1]
	v_mov_b32_e32 v128, v60
	v_mov_b32_e32 v129, v61
	v_pk_mul_f32 v[60:61], v[22:23], v[36:37]
	v_mov_b32_e32 v12, v7
	v_accvgpr_write_b32 a21, v29
	v_mov_b32_dpp v25, v70 row_shl:1 row_mask:0xf bank_mask:0xf
	v_pk_fma_f32 v[60:61], v[70:71], v[118:119], v[60:61] op_sel_hi:[0,1,1]
	v_mov_b32_e32 v62, v71
	v_mov_b32_e32 v63, v107
	v_mov_b32_dpp v12, v73 row_shr:1 row_mask:0xf bank_mask:0xf
	v_accvgpr_read_b32 v28, a26
	v_mov_b32_e32 v29, v73
	v_accvgpr_read_b32 v121, a3
	v_pk_fma_f32 v[60:61], v[62:63], v[24:25], v[60:61]
	v_pk_mul_f32 v[62:63], v[28:29], v[12:13]
	v_accvgpr_read_b32 v120, a2
	v_mov_b32_dpp v7, v72 row_shl:1 row_mask:0xf bank_mask:0xf
	v_pk_fma_f32 v[62:63], v[72:73], v[120:121], v[62:63] op_sel_hi:[0,1,1]
	v_mov_b32_e32 v68, v73
	v_mov_b32_e32 v69, v101
	v_mov_b32_e32 v78, v21
	v_pk_fma_f32 v[62:63], v[68:69], v[6:7], v[62:63]
	v_pk_add_f32 v[60:61], v[60:61], 0 op_sel_hi:[1,0]
	v_mov_b32_dpp v78, v83 row_shr:1 row_mask:0xf bank_mask:0xf
	v_mov_b32_e32 v53, v83
	v_accvgpr_read_b32 v125, a19
	v_pk_add_f32 v[60:61], v[60:61], v[62:63]
	v_pk_mul_f32 v[62:63], v[52:53], v[78:79]
	v_accvgpr_read_b32 v124, a18
	v_mov_b32_dpp v21, v82 row_shl:1 row_mask:0xf bank_mask:0xf
	v_pk_fma_f32 v[62:63], v[82:83], v[124:125], v[62:63] op_sel_hi:[0,1,1]
	v_mov_b32_e32 v68, v83
	v_mov_b32_e32 v69, v5
	v_pk_fma_f32 v[62:63], v[68:69], v[20:21], v[62:63]
	v_mov_b32_e32 v76, v11
	v_pk_add_f32 v[60:61], v[60:61], v[62:63]
	s_mov_b64 s[0:1], 0xc10000
	v_mov_b32_dpp v76, v81 row_shr:1 row_mask:0xf bank_mask:0xf
	v_mov_b32_e32 v41, v81
	v_accvgpr_read_b32 v123, a37
	v_accvgpr_read_b32 v4, a14
	v_lshl_add_u64 v[136:137], v[134:135], 0, s[0:1]
	s_nop 1
	s_mov_b64 vcc, s[28:29]
	s_nop 0
	v_cndmask_b32_dpp v130, v60, v128, vcc quad_perm:[1,0,3,2] row_mask:0xf bank_mask:0xf
	v_cndmask_b32_dpp v131, v61, v129, vcc quad_perm:[1,0,3,2] row_mask:0xf bank_mask:0xf
	s_mov_b64 vcc, s[30:31]
	s_nop 0
	v_cndmask_b32_dpp v132, v128, v60, vcc quad_perm:[1,0,3,2] row_mask:0xf bank_mask:0xf
	v_cndmask_b32_dpp v133, v129, v61, vcc quad_perm:[1,0,3,2] row_mask:0xf bank_mask:0xf
	global_store_dwordx4 v[136:137], v[130:133], off sc0 sc1 nt
	s_nop 1
	v_pk_mul_f32 v[60:61], v[40:41], v[76:77]
	v_accvgpr_read_b32 v122, a36
	v_accvgpr_read_b32 v5, a15
	v_mov_b32_e32 v2, v35
	v_accvgpr_mov_b32 a32, a24
	v_accvgpr_write_b32 a24, v22
	v_mov_b64_e32 v[22:23], v[118:119]
	v_mov_b32_dpp v11, v80 row_shl:1 row_mask:0xf bank_mask:0xf
	v_pk_fma_f32 v[60:61], v[80:81], v[122:123], v[60:61] op_sel_hi:[0,1,1]
	v_pk_mov_b32 v[62:63], v[80:81], v[4:5] op_sel:[1,0]
	v_mov_b32_dpp v2, v85 row_shr:1 row_mask:0xf bank_mask:0xf
	v_mov_b32_e32 v106, v0
	v_mov_b32_e32 v107, v85
	v_accvgpr_read_b32 v119, a11
	v_pk_fma_f32 v[60:61], v[62:63], v[10:11], v[60:61]
	v_pk_mul_f32 v[62:63], v[106:107], v[2:3]
	v_accvgpr_read_b32 v118, a10
	v_mov_b64_e32 v[100:101], v[14:15]
	v_mov_b32_dpp v35, v84 row_shl:1 row_mask:0xf bank_mask:0xf
	v_pk_fma_f32 v[62:63], v[84:85], v[118:119], v[62:63] op_sel_hi:[0,1,1]
	v_pk_mov_b32 v[68:69], v[84:85], v[100:101] op_sel:[1,0]
	v_mov_b32_e32 v92, v59
	v_accvgpr_write_b32 a26, v52
	v_mov_b32_e32 v74, v40
	v_pk_fma_f32 v[62:63], v[68:69], v[34:35], v[62:63]
	v_pk_add_f32 v[60:61], v[60:61], 0 op_sel_hi:[1,0]
	v_mov_b32_dpp v92, v117 row_shr:1 row_mask:0xf bank_mask:0xf
	v_mov_b32_e32 v97, v117
	v_accvgpr_read_b32 v41, a31
	v_accvgpr_read_b32 v53, a45
	v_pk_add_f32 v[60:61], v[60:61], v[62:63]
	v_pk_mul_f32 v[62:63], v[96:97], v[92:93]
	v_accvgpr_read_b32 v40, a30
	v_accvgpr_read_b32 v52, a44
	v_mov_b32_dpp v59, v116 row_shl:1 row_mask:0xf bank_mask:0xf
	v_pk_fma_f32 v[62:63], v[116:117], v[40:41], v[62:63] op_sel_hi:[0,1,1]
	v_pk_mov_b32 v[68:69], v[116:117], v[52:53] op_sel:[1,0]
	v_mov_b32_e32 v94, v57
	v_pk_fma_f32 v[62:63], v[68:69], v[58:59], v[62:63]
	s_mov_b64 s[0:1], 0xc20000
	v_pk_add_f32 v[60:61], v[60:61], v[62:63]
	v_mov_b32_dpp v94, v115 row_shr:1 row_mask:0xf bank_mask:0xf
	v_mov_b32_e32 v99, v115
	v_accvgpr_read_b32 v14, a20
	v_lshl_add_u64 v[62:63], v[54:55], 0, s[0:1]
	v_mov_b32_e32 v128, v60
	v_mov_b32_e32 v129, v61
	v_pk_mul_f32 v[60:61], v[98:99], v[94:95]
	v_accvgpr_read_b32 v15, a21
	v_mov_b32_e32 v102, v51
	v_mov_b32_dpp v57, v114 row_shl:1 row_mask:0xf bank_mask:0xf
	v_pk_fma_f32 v[60:61], v[114:115], v[14:15], v[60:61] op_sel_hi:[0,1,1]
	v_mov_b32_e32 v62, v115
	v_mov_b32_e32 v63, v5
	v_mov_b32_dpp v102, v113 row_shr:1 row_mask:0xf bank_mask:0xf
	v_mov_b32_e32 v105, v113
	v_pk_fma_f32 v[60:61], v[62:63], v[56:57], v[60:61]
	v_pk_mul_f32 v[62:63], v[104:105], v[102:103]
	v_accvgpr_write_b32 a8, v8
	v_mov_b32_dpp v51, v112 row_shl:1 row_mask:0xf bank_mask:0xf
	v_pk_fma_f32 v[62:63], v[112:113], v[16:17], v[62:63] op_sel_hi:[0,1,1]
	v_mov_b32_e32 v68, v113
	v_mov_b32_e32 v69, v101
	v_mov_b32_e32 v108, v49
	v_accvgpr_write_b32 a9, v9
	v_pk_fma_f32 v[62:63], v[68:69], v[50:51], v[62:63]
	v_pk_add_f32 v[60:61], v[60:61], 0 op_sel_hi:[1,0]
	v_mov_b32_dpp v108, v91 row_shr:1 row_mask:0xf bank_mask:0xf
	v_mov_b32_e32 v111, v91
	v_accvgpr_read_b32 v8, a22
	v_pk_add_f32 v[60:61], v[60:61], v[62:63]
	v_pk_mul_f32 v[62:63], v[110:111], v[108:109]
	v_accvgpr_read_b32 v9, a23
	v_mov_b32_dpp v49, v90 row_shl:1 row_mask:0xf bank_mask:0xf
	v_pk_fma_f32 v[62:63], v[90:91], v[8:9], v[62:63] op_sel_hi:[0,1,1]
	v_mov_b32_e32 v68, v91
	v_mov_b32_e32 v69, v53
	v_pk_fma_f32 v[62:63], v[68:69], v[48:49], v[62:63]
	s_mov_b64 s[0:1], 0xc30000
	v_pk_add_f32 v[60:61], v[60:61], v[62:63]
	v_lshl_add_u64 v[136:137], v[134:135], 0, s[0:1]
	s_nop 1
	s_mov_b64 vcc, s[28:29]
	s_nop 0
	v_cndmask_b32_dpp v130, v60, v128, vcc quad_perm:[1,0,3,2] row_mask:0xf bank_mask:0xf
	v_cndmask_b32_dpp v131, v61, v129, vcc quad_perm:[1,0,3,2] row_mask:0xf bank_mask:0xf
	s_mov_b64 vcc, s[30:31]
	s_nop 0
	v_cndmask_b32_dpp v132, v128, v60, vcc quad_perm:[1,0,3,2] row_mask:0xf bank_mask:0xf
	v_cndmask_b32_dpp v133, v129, v61, vcc quad_perm:[1,0,3,2] row_mask:0xf bank_mask:0xf
	global_store_dwordx4 v[136:137], v[130:133], off sc0 sc1 nt
	s_nop 1
	s_waitcnt vmcnt(20)
	v_accvgpr_write_b32 a16, v88
	v_accvgpr_write_b32 a10, v100
	s_waitcnt lgkmcnt(0)
	s_barrier
	v_add_u32_e32 v2, 0xe010, v31
	v_add_u32_e32 v5, 0xe000, v66
	ds_read_b64 v[60:61], v2
	ds_read_b64 v[62:63], v2 offset:288
	ds_read_b64 v[68:69], v2 offset:576
	ds_read_b64 v[70:71], v2 offset:1728
	ds_read_b64 v[72:73], v2 offset:2016
	ds_read_b64 v[82:83], v2 offset:2304
	ds_read_b64 v[80:81], v2 offset:3456
	ds_read_b64 v[84:85], v2 offset:3744
	ds_read_b64 v[116:117], v2 offset:4032
	ds_read_b64 v[114:115], v2 offset:5184
	ds_read_b64 v[112:113], v2 offset:5472
	ds_read_b64 v[90:91], v2 offset:5760
	ds_read_b32 v43, v5
	ds_read_b32 v19, v5 offset:288
	ds_read_b32 v39, v5 offset:576
	ds_read_b32 v25, v5 offset:1728
	ds_read_b32 v7, v5 offset:2016
	ds_read_b32 v21, v5 offset:2304
	ds_read_b32 v11, v5 offset:3456
	ds_read_b32 v35, v5 offset:3744
	ds_read_b32 v59, v5 offset:4032
	ds_read_b32 v57, v5 offset:5184
	ds_read_b32 v51, v5 offset:5472
	ds_read_b32 v49, v5 offset:5760
	s_waitcnt lgkmcnt(0)
	v_accvgpr_write_b32 a17, v89
	v_mov_b32_e32 v46, v43
	v_accvgpr_write_b32 a11, v101
	v_mov_b32_e32 v33, v61
	v_mov_b32_dpp v46, v61 row_shr:1 row_mask:0xf bank_mask:0xf
	v_accvgpr_read_b32 v89, a9
	v_accvgpr_read_b32 v101, a39
	v_pk_mul_f32 v[86:87], v[32:33], v[46:47]
	v_accvgpr_read_b32 v88, a8
	v_accvgpr_read_b32 v100, a38
	v_mov_b32_e32 v26, v19
	v_accvgpr_write_b32 a19, v17
	v_mov_b32_dpp v43, v60 row_shl:1 row_mask:0xf bank_mask:0xf
	v_pk_fma_f32 v[86:87], v[60:61], v[88:89], v[86:87] op_sel_hi:[0,1,1]
	v_pk_mov_b32 v[60:61], v[60:61], v[100:101] op_sel:[1,0]
	v_mov_b32_dpp v26, v63 row_shr:1 row_mask:0xf bank_mask:0xf
	v_accvgpr_read_b32 v0, a32
	v_mov_b32_e32 v1, v63
	v_accvgpr_read_b32 v4, a34
	v_accvgpr_write_b32 a18, v16
	v_pk_fma_f32 v[60:61], v[60:61], v[42:43], v[86:87]
	v_pk_mul_f32 v[86:87], v[0:1], v[26:27]
	v_mov_b64_e32 v[16:17], v[126:127]
	v_accvgpr_read_b32 v5, a35
	v_mov_b32_dpp v19, v62 row_shl:1 row_mask:0xf bank_mask:0xf
	v_pk_fma_f32 v[86:87], v[62:63], v[16:17], v[86:87] op_sel_hi:[0,1,1]
	v_pk_mov_b32 v[62:63], v[62:63], v[4:5] op_sel:[1,0]
	v_mov_b32_e32 v44, v39
	v_accvgpr_read_b32 v30, a48
	v_mov_b32_e32 v64, v28
	v_accvgpr_write_b32 a7, v66
	v_pk_fma_f32 v[62:63], v[62:63], v[18:19], v[86:87]
	v_pk_add_f32 v[60:61], v[60:61], 0 op_sel_hi:[1,0]
	v_mov_b32_dpp v44, v69 row_shr:1 row_mask:0xf bank_mask:0xf
	v_mov_b32_e32 v31, v69
	v_accvgpr_read_b32 v29, a17
	v_accvgpr_read_b32 v67, a47
	v_pk_add_f32 v[60:61], v[60:61], v[62:63]
	v_pk_mul_f32 v[62:63], v[30:31], v[44:45]
	v_accvgpr_read_b32 v28, a16
	v_accvgpr_read_b32 v66, a46
	v_mov_b32_dpp v39, v68 row_shl:1 row_mask:0xf bank_mask:0xf
	v_pk_fma_f32 v[62:63], v[68:69], v[28:29], v[62:63] op_sel_hi:[0,1,1]
	v_pk_mov_b32 v[68:69], v[68:69], v[66:67] op_sel:[1,0]
	v_mov_b32_e32 v36, v25
	v_pk_fma_f32 v[62:63], v[68:69], v[38:39], v[62:63]
	s_mov_b64 s[0:1], 0x1000000
	v_pk_add_f32 v[60:61], v[60:61], v[62:63]
	v_mov_b32_dpp v36, v71 row_shr:1 row_mask:0xf bank_mask:0xf
	v_accvgpr_read_b32 v126, a24
	v_mov_b32_e32 v127, v71
	v_lshl_add_u64 v[62:63], v[54:55], 0, s[0:1]
	v_mov_b32_e32 v128, v60
	v_mov_b32_e32 v129, v61
	v_pk_mul_f32 v[60:61], v[126:127], v[36:37]
	v_mov_b32_e32 v12, v7
	v_mov_b32_dpp v25, v70 row_shl:1 row_mask:0xf bank_mask:0xf
	v_pk_fma_f32 v[60:61], v[70:71], v[22:23], v[60:61] op_sel_hi:[0,1,1]
	v_mov_b32_e32 v62, v71
	v_mov_b32_e32 v63, v101
	v_mov_b32_dpp v12, v73 row_shr:1 row_mask:0xf bank_mask:0xf
	v_mov_b32_e32 v52, v64
	v_mov_b32_e32 v53, v73
	v_pk_fma_f32 v[60:61], v[62:63], v[24:25], v[60:61]
	v_pk_mul_f32 v[62:63], v[52:53], v[12:13]
	v_mov_b32_dpp v7, v72 row_shl:1 row_mask:0xf bank_mask:0xf
	v_pk_fma_f32 v[62:63], v[72:73], v[120:121], v[62:63] op_sel_hi:[0,1,1]
	v_mov_b32_e32 v68, v73
	v_mov_b32_e32 v69, v5
	v_mov_b32_e32 v78, v21
	v_pk_fma_f32 v[62:63], v[68:69], v[6:7], v[62:63]
	v_pk_add_f32 v[60:61], v[60:61], 0 op_sel_hi:[1,0]
	v_mov_b32_dpp v78, v83 row_shr:1 row_mask:0xf bank_mask:0xf
	v_accvgpr_read_b32 v4, a26
	v_mov_b32_e32 v5, v83
	v_pk_add_f32 v[60:61], v[60:61], v[62:63]
	v_pk_mul_f32 v[62:63], v[4:5], v[78:79]
	v_mov_b32_dpp v21, v82 row_shl:1 row_mask:0xf bank_mask:0xf
	v_pk_fma_f32 v[62:63], v[82:83], v[124:125], v[62:63] op_sel_hi:[0,1,1]
	v_mov_b32_e32 v68, v83
	v_mov_b32_e32 v69, v67
	v_accvgpr_write_b32 a8, v120
	v_pk_fma_f32 v[62:63], v[68:69], v[20:21], v[62:63]
	v_mov_b32_e32 v76, v11
	v_accvgpr_write_b32 a9, v121
	v_pk_add_f32 v[60:61], v[60:61], v[62:63]
	s_mov_b64 s[0:1], 0x1010000
	v_mov_b32_dpp v76, v81 row_shr:1 row_mask:0xf bank_mask:0xf
	v_mov_b32_e32 v120, v74
	v_mov_b32_e32 v121, v81
	v_accvgpr_read_b32 v101, a15
	v_accvgpr_mov_b32 a12, a38
	v_lshl_add_u64 v[136:137], v[134:135], 0, s[0:1]
	s_nop 1
	s_mov_b64 vcc, s[28:29]
	s_nop 0
	v_cndmask_b32_dpp v130, v60, v128, vcc quad_perm:[1,0,3,2] row_mask:0xf bank_mask:0xf
	v_cndmask_b32_dpp v131, v61, v129, vcc quad_perm:[1,0,3,2] row_mask:0xf bank_mask:0xf
	s_mov_b64 vcc, s[30:31]
	s_nop 0
	v_cndmask_b32_dpp v132, v128, v60, vcc quad_perm:[1,0,3,2] row_mask:0xf bank_mask:0xf
	v_cndmask_b32_dpp v133, v129, v61, vcc quad_perm:[1,0,3,2] row_mask:0xf bank_mask:0xf
	global_store_dwordx4 v[136:137], v[130:133], off sc0 sc1 nt
	s_nop 1
	v_pk_mul_f32 v[60:61], v[120:121], v[76:77]
	v_accvgpr_read_b32 v100, a14
	v_mov_b32_e32 v2, v35
	v_accvgpr_mov_b32 a13, a39
	v_accvgpr_write_b32 a20, v22
	v_mov_b32_dpp v11, v80 row_shl:1 row_mask:0xf bank_mask:0xf
	v_pk_fma_f32 v[60:61], v[80:81], v[122:123], v[60:61] op_sel_hi:[0,1,1]
	v_pk_mov_b32 v[62:63], v[80:81], v[100:101] op_sel:[1,0]
	v_mov_b32_dpp v2, v85 row_shr:1 row_mask:0xf bank_mask:0xf
	v_mov_b32_e32 v107, v85
	v_accvgpr_read_b32 v123, a11
	v_accvgpr_write_b32 a21, v23
	v_accvgpr_read_b32 v23, a13
	v_pk_fma_f32 v[60:61], v[62:63], v[10:11], v[60:61]
	v_pk_mul_f32 v[62:63], v[106:107], v[2:3]
	v_accvgpr_read_b32 v122, a10
	v_accvgpr_read_b32 v22, a12
	v_mov_b32_dpp v35, v84 row_shl:1 row_mask:0xf bank_mask:0xf
	v_pk_fma_f32 v[62:63], v[84:85], v[118:119], v[62:63] op_sel_hi:[0,1,1]
	v_accvgpr_write_b32 a12, v118
	v_pk_mov_b32 v[68:69], v[84:85], v[122:123] op_sel:[1,0]
	v_mov_b32_e32 v92, v59
	v_accvgpr_write_b32 a13, v119
	v_pk_fma_f32 v[62:63], v[68:69], v[34:35], v[62:63]
	v_pk_add_f32 v[60:61], v[60:61], 0 op_sel_hi:[1,0]
	v_mov_b32_dpp v92, v117 row_shr:1 row_mask:0xf bank_mask:0xf
	v_mov_b32_e32 v97, v117
	v_mov_b64_e32 v[118:119], v[40:41]
	v_accvgpr_read_b32 v40, a44
	v_pk_add_f32 v[60:61], v[60:61], v[62:63]
	v_pk_mul_f32 v[62:63], v[96:97], v[92:93]
	v_accvgpr_read_b32 v41, a45
	v_mov_b32_dpp v59, v116 row_shl:1 row_mask:0xf bank_mask:0xf
	v_pk_fma_f32 v[62:63], v[116:117], v[118:119], v[62:63] op_sel_hi:[0,1,1]
	v_pk_mov_b32 v[68:69], v[116:117], v[40:41] op_sel:[1,0]
	v_mov_b32_e32 v94, v57
	v_pk_fma_f32 v[62:63], v[68:69], v[58:59], v[62:63]
	s_mov_b64 s[0:1], 0x1020000
	v_pk_add_f32 v[60:61], v[60:61], v[62:63]
	v_mov_b32_dpp v94, v115 row_shr:1 row_mask:0xf bank_mask:0xf
	v_mov_b32_e32 v99, v115
	v_lshl_add_u64 v[62:63], v[54:55], 0, s[0:1]
	v_mov_b32_e32 v128, v60
	v_mov_b32_e32 v129, v61
	v_pk_mul_f32 v[60:61], v[98:99], v[94:95]
	v_mov_b32_e32 v102, v51
	v_accvgpr_write_b32 a30, v4
	v_mov_b32_dpp v57, v114 row_shl:1 row_mask:0xf bank_mask:0xf
	v_pk_fma_f32 v[60:61], v[114:115], v[14:15], v[60:61] op_sel_hi:[0,1,1]
	v_mov_b32_e32 v62, v115
	v_mov_b32_e32 v63, v101
	v_mov_b32_dpp v102, v113 row_shr:1 row_mask:0xf bank_mask:0xf
	v_mov_b32_e32 v105, v113
	v_accvgpr_read_b32 v4, a18
	v_pk_fma_f32 v[60:61], v[62:63], v[56:57], v[60:61]
	v_pk_mul_f32 v[62:63], v[104:105], v[102:103]
	v_accvgpr_read_b32 v5, a19
	v_mov_b32_dpp v51, v112 row_shl:1 row_mask:0xf bank_mask:0xf
	v_pk_fma_f32 v[62:63], v[112:113], v[4:5], v[62:63] op_sel_hi:[0,1,1]
	v_mov_b32_e32 v68, v113
	v_mov_b32_e32 v69, v123
	v_mov_b32_e32 v108, v49
	v_pk_fma_f32 v[62:63], v[68:69], v[50:51], v[62:63]
	v_pk_add_f32 v[60:61], v[60:61], 0 op_sel_hi:[1,0]
	v_mov_b32_dpp v108, v91 row_shr:1 row_mask:0xf bank_mask:0xf
	v_mov_b32_e32 v111, v91
	v_pk_add_f32 v[60:61], v[60:61], v[62:63]
	v_pk_mul_f32 v[62:63], v[110:111], v[108:109]
	v_mov_b32_dpp v49, v90 row_shl:1 row_mask:0xf bank_mask:0xf
	v_pk_fma_f32 v[62:63], v[90:91], v[8:9], v[62:63] op_sel_hi:[0,1,1]
	v_mov_b32_e32 v68, v91
	v_mov_b32_e32 v69, v41
	v_pk_fma_f32 v[62:63], v[68:69], v[48:49], v[62:63]
	s_mov_b64 s[0:1], 0x1030000
	v_pk_add_f32 v[60:61], v[60:61], v[62:63]
	v_lshl_add_u64 v[136:137], v[134:135], 0, s[0:1]
	s_nop 1
	s_mov_b64 vcc, s[28:29]
	s_nop 0
	v_cndmask_b32_dpp v130, v60, v128, vcc quad_perm:[1,0,3,2] row_mask:0xf bank_mask:0xf
	v_cndmask_b32_dpp v131, v61, v129, vcc quad_perm:[1,0,3,2] row_mask:0xf bank_mask:0xf
	s_mov_b64 vcc, s[30:31]
	s_nop 0
	v_cndmask_b32_dpp v132, v128, v60, vcc quad_perm:[1,0,3,2] row_mask:0xf bank_mask:0xf
	v_cndmask_b32_dpp v133, v129, v61, vcc quad_perm:[1,0,3,2] row_mask:0xf bank_mask:0xf
	global_store_dwordx4 v[136:137], v[130:133], off sc0 sc1 nt
	s_nop 1
	s_waitcnt vmcnt(16)
	s_waitcnt lgkmcnt(0)
	s_barrier
	v_accvgpr_read_b32 v2, a0
	v_accvgpr_read_b32 v8, a4
	ds_read_b64 v[60:61], v8
	ds_read_b64 v[62:63], v8 offset:288
	ds_read_b64 v[68:69], v8 offset:576
	ds_read_b64 v[70:71], v8 offset:1728
	ds_read_b64 v[72:73], v8 offset:2016
	ds_read_b64 v[82:83], v8 offset:2304
	ds_read_b64 v[80:81], v8 offset:3456
	ds_read_b64 v[84:85], v8 offset:3744
	ds_read_b64 v[116:117], v8 offset:4032
	ds_read_b64 v[114:115], v8 offset:5184
	ds_read_b64 v[112:113], v8 offset:5472
	ds_read_b64 v[90:91], v8 offset:5760
	ds_read_b32 v43, v2
	ds_read_b32 v19, v2 offset:288
	ds_read_b32 v39, v2 offset:576
	ds_read_b32 v25, v2 offset:1728
	ds_read_b32 v7, v2 offset:2016
	ds_read_b32 v21, v2 offset:2304
	ds_read_b32 v11, v2 offset:3456
	ds_read_b32 v35, v2 offset:3744
	ds_read_b32 v59, v2 offset:4032
	ds_read_b32 v57, v2 offset:5184
	ds_read_b32 v51, v2 offset:5472
	ds_read_b32 v49, v2 offset:5760
	s_waitcnt lgkmcnt(0)
	v_mov_b32_e32 v64, v32
	v_mov_b32_e32 v46, v43
	v_mov_b32_e32 v65, v61
	v_mov_b64_e32 v[100:101], v[22:23]
	v_mov_b32_dpp v46, v61 row_shr:1 row_mask:0xf bank_mask:0xf
	v_pk_mul_f32 v[86:87], v[64:65], v[46:47]
	v_mov_b32_e32 v26, v19
	v_mov_b32_dpp v43, v60 row_shl:1 row_mask:0xf bank_mask:0xf
	v_pk_fma_f32 v[86:87], v[60:61], v[88:89], v[86:87] op_sel_hi:[0,1,1]
	v_pk_mov_b32 v[60:61], v[60:61], v[100:101] op_sel:[1,0]
	v_mov_b32_dpp v26, v63 row_shr:1 row_mask:0xf bank_mask:0xf
	v_mov_b32_e32 v1, v63
	v_accvgpr_read_b32 v67, a35
	v_pk_fma_f32 v[60:61], v[60:61], v[42:43], v[86:87]
	v_pk_mul_f32 v[86:87], v[0:1], v[26:27]
	v_accvgpr_read_b32 v66, a34
	v_accvgpr_write_b32 a10, v14
	v_mov_b32_dpp v19, v62 row_shl:1 row_mask:0xf bank_mask:0xf
	v_pk_fma_f32 v[86:87], v[62:63], v[16:17], v[86:87] op_sel_hi:[0,1,1]
	v_pk_mov_b32 v[62:63], v[62:63], v[66:67] op_sel:[1,0]
	v_mov_b32_e32 v44, v39
	v_accvgpr_write_b32 a11, v15
	v_pk_fma_f32 v[62:63], v[62:63], v[18:19], v[86:87]
	v_pk_add_f32 v[60:61], v[60:61], 0 op_sel_hi:[1,0]
	v_mov_b32_dpp v44, v69 row_shr:1 row_mask:0xf bank_mask:0xf
	v_mov_b32_e32 v31, v69
	v_accvgpr_read_b32 v14, a16
	v_accvgpr_read_b32 v28, a46
	v_pk_add_f32 v[60:61], v[60:61], v[62:63]
	v_pk_mul_f32 v[62:63], v[30:31], v[44:45]
	v_accvgpr_read_b32 v15, a17
	v_accvgpr_read_b32 v29, a47
	v_mov_b32_dpp v39, v68 row_shl:1 row_mask:0xf bank_mask:0xf
	v_pk_fma_f32 v[62:63], v[68:69], v[14:15], v[62:63] op_sel_hi:[0,1,1]
	v_pk_mov_b32 v[68:69], v[68:69], v[28:29] op_sel:[1,0]
	v_mov_b32_e32 v36, v25
	v_pk_fma_f32 v[62:63], v[68:69], v[38:39], v[62:63]
	s_mov_b64 s[0:1], 0x1400000
	v_pk_add_f32 v[60:61], v[60:61], v[62:63]
	v_mov_b32_dpp v36, v71 row_shr:1 row_mask:0xf bank_mask:0xf
	v_mov_b32_e32 v127, v71
	v_accvgpr_read_b32 v8, a20
	v_lshl_add_u64 v[62:63], v[54:55], 0, s[0:1]
	v_mov_b32_e32 v128, v60
	v_mov_b32_e32 v129, v61
	v_pk_mul_f32 v[60:61], v[126:127], v[36:37]
	v_accvgpr_read_b32 v9, a21
	v_accvgpr_write_b32 a25, v23
	v_mov_b32_e32 v12, v7
	v_mov_b32_dpp v25, v70 row_shl:1 row_mask:0xf bank_mask:0xf
	v_pk_fma_f32 v[60:61], v[70:71], v[8:9], v[60:61] op_sel_hi:[0,1,1]
	v_mov_b32_e32 v62, v71
	v_mov_b32_e32 v63, v101
	v_accvgpr_write_b32 a24, v22
	v_mov_b32_dpp v12, v73 row_shr:1 row_mask:0xf bank_mask:0xf
	v_mov_b32_e32 v74, v52
	v_mov_b32_e32 v75, v73
	v_accvgpr_read_b32 v23, a9
	v_accvgpr_write_b32 a26, v124
	v_accvgpr_mov_b32 a2, a22
	v_pk_fma_f32 v[60:61], v[62:63], v[24:25], v[60:61]
	v_pk_mul_f32 v[62:63], v[74:75], v[12:13]
	v_accvgpr_read_b32 v22, a8
	v_accvgpr_write_b32 a27, v125
	v_accvgpr_mov_b32 a3, a23
	v_accvgpr_write_b32 a22, v88
	v_mov_b32_dpp v7, v72 row_shl:1 row_mask:0xf bank_mask:0xf
	v_pk_fma_f32 v[62:63], v[72:73], v[22:23], v[62:63] op_sel_hi:[0,1,1]
	v_mov_b32_e32 v68, v73
	v_mov_b32_e32 v69, v67
	v_mov_b32_e32 v78, v21
	v_accvgpr_write_b32 a23, v89
	v_pk_fma_f32 v[62:63], v[68:69], v[6:7], v[62:63]
	v_pk_add_f32 v[60:61], v[60:61], 0 op_sel_hi:[1,0]
	v_mov_b32_dpp v78, v83 row_shr:1 row_mask:0xf bank_mask:0xf
	v_accvgpr_read_b32 v52, a30
	v_mov_b32_e32 v53, v83
	v_accvgpr_read_b32 v89, a27
	v_pk_add_f32 v[60:61], v[60:61], v[62:63]
	v_pk_mul_f32 v[62:63], v[52:53], v[78:79]
	v_accvgpr_read_b32 v88, a26
	v_mov_b32_dpp v21, v82 row_shl:1 row_mask:0xf bank_mask:0xf
	v_pk_fma_f32 v[62:63], v[82:83], v[88:89], v[62:63] op_sel_hi:[0,1,1]
	v_mov_b32_e32 v68, v83
	v_mov_b32_e32 v69, v29
	v_pk_fma_f32 v[62:63], v[68:69], v[20:21], v[62:63]
	v_mov_b32_e32 v76, v11
	v_accvgpr_read_b32 v125, a37
	v_pk_add_f32 v[60:61], v[60:61], v[62:63]
	s_mov_b64 s[0:1], 0x1410000
	v_mov_b32_dpp v76, v81 row_shr:1 row_mask:0xf bank_mask:0xf
	v_mov_b32_e32 v121, v81
	v_accvgpr_read_b32 v101, a15
	v_accvgpr_read_b32 v124, a36
	v_lshl_add_u64 v[136:137], v[134:135], 0, s[0:1]
	s_nop 1
	s_mov_b64 vcc, s[28:29]
	s_nop 0
	v_cndmask_b32_dpp v130, v60, v128, vcc quad_perm:[1,0,3,2] row_mask:0xf bank_mask:0xf
	v_cndmask_b32_dpp v131, v61, v129, vcc quad_perm:[1,0,3,2] row_mask:0xf bank_mask:0xf
	s_mov_b64 vcc, s[30:31]
	s_nop 0
	v_cndmask_b32_dpp v132, v128, v60, vcc quad_perm:[1,0,3,2] row_mask:0xf bank_mask:0xf
	v_cndmask_b32_dpp v133, v129, v61, vcc quad_perm:[1,0,3,2] row_mask:0xf bank_mask:0xf
	global_store_dwordx4 v[136:137], v[130:133], off sc0 sc1 nt
	s_nop 1
	v_pk_mul_f32 v[60:61], v[120:121], v[76:77]
	v_accvgpr_read_b32 v100, a14
	v_mov_b32_e32 v2, v35
	v_mov_b32_dpp v11, v80 row_shl:1 row_mask:0xf bank_mask:0xf
	v_pk_fma_f32 v[60:61], v[80:81], v[124:125], v[60:61] op_sel_hi:[0,1,1]
	v_pk_mov_b32 v[62:63], v[80:81], v[100:101] op_sel:[1,0]
	v_mov_b32_dpp v2, v85 row_shr:1 row_mask:0xf bank_mask:0xf
	v_mov_b32_e32 v107, v85
	v_accvgpr_read_b32 v29, a13
	v_pk_fma_f32 v[60:61], v[62:63], v[10:11], v[60:61]
	v_pk_mul_f32 v[62:63], v[106:107], v[2:3]
	v_accvgpr_read_b32 v28, a12
	v_mov_b32_dpp v35, v84 row_shl:1 row_mask:0xf bank_mask:0xf
	v_pk_fma_f32 v[62:63], v[84:85], v[28:29], v[62:63] op_sel_hi:[0,1,1]
	v_pk_mov_b32 v[68:69], v[84:85], v[122:123] op_sel:[1,0]
	v_mov_b32_e32 v92, v59
	v_pk_fma_f32 v[62:63], v[68:69], v[34:35], v[62:63]
	v_pk_add_f32 v[60:61], v[60:61], 0 op_sel_hi:[1,0]
	v_mov_b32_dpp v92, v117 row_shr:1 row_mask:0xf bank_mask:0xf
	v_mov_b32_e32 v97, v117
	v_pk_add_f32 v[60:61], v[60:61], v[62:63]
	v_pk_mul_f32 v[62:63], v[96:97], v[92:93]
	v_accvgpr_write_b32 a8, v118
	v_pk_fma_f32 v[62:63], v[116:117], v[118:119], v[62:63] op_sel_hi:[0,1,1]
	v_accvgpr_write_b32 a9, v119
	v_accvgpr_read_b32 v119, a45
	v_accvgpr_read_b32 v118, a44
	v_mov_b32_dpp v59, v116 row_shl:1 row_mask:0xf bank_mask:0xf
	v_pk_mov_b32 v[68:69], v[116:117], v[118:119] op_sel:[1,0]
	v_mov_b32_e32 v94, v57
	v_pk_fma_f32 v[62:63], v[68:69], v[58:59], v[62:63]
	s_mov_b64 s[0:1], 0x1420000
	v_pk_add_f32 v[60:61], v[60:61], v[62:63]
	v_mov_b32_dpp v94, v115 row_shr:1 row_mask:0xf bank_mask:0xf
	v_mov_b32_e32 v99, v115
	v_accvgpr_read_b32 v41, a11
	v_lshl_add_u64 v[62:63], v[54:55], 0, s[0:1]
	v_mov_b32_e32 v128, v60
	v_mov_b32_e32 v129, v61
	v_pk_mul_f32 v[60:61], v[98:99], v[94:95]
	v_accvgpr_read_b32 v40, a10
	v_mov_b32_e32 v102, v51
	v_mov_b32_dpp v57, v114 row_shl:1 row_mask:0xf bank_mask:0xf
	v_pk_fma_f32 v[60:61], v[114:115], v[40:41], v[60:61] op_sel_hi:[0,1,1]
	v_mov_b32_e32 v62, v115
	v_mov_b32_e32 v63, v101
	v_mov_b32_dpp v102, v113 row_shr:1 row_mask:0xf bank_mask:0xf
	v_mov_b32_e32 v105, v113
	v_pk_fma_f32 v[60:61], v[62:63], v[56:57], v[60:61]
	v_pk_mul_f32 v[62:63], v[104:105], v[102:103]
	v_mov_b32_dpp v51, v112 row_shl:1 row_mask:0xf bank_mask:0xf
	v_pk_fma_f32 v[62:63], v[112:113], v[4:5], v[62:63] op_sel_hi:[0,1,1]
	v_mov_b32_e32 v68, v113
	v_mov_b32_e32 v69, v123
	v_mov_b32_e32 v108, v49
	v_pk_fma_f32 v[62:63], v[68:69], v[50:51], v[62:63]
	v_pk_add_f32 v[60:61], v[60:61], 0 op_sel_hi:[1,0]
	v_mov_b32_dpp v108, v91 row_shr:1 row_mask:0xf bank_mask:0xf
	v_mov_b32_e32 v111, v91
	v_accvgpr_read_b32 v5, a3
	v_pk_add_f32 v[60:61], v[60:61], v[62:63]
	v_pk_mul_f32 v[62:63], v[110:111], v[108:109]
	v_accvgpr_read_b32 v4, a2
	v_mov_b32_dpp v49, v90 row_shl:1 row_mask:0xf bank_mask:0xf
	v_pk_fma_f32 v[62:63], v[90:91], v[4:5], v[62:63] op_sel_hi:[0,1,1]
	v_mov_b32_e32 v68, v91
	v_mov_b32_e32 v69, v119
	v_pk_fma_f32 v[62:63], v[68:69], v[48:49], v[62:63]
	s_mov_b64 s[0:1], 0x1430000
	v_pk_add_f32 v[60:61], v[60:61], v[62:63]
	v_lshl_add_u64 v[136:137], v[134:135], 0, s[0:1]
	s_nop 1
	s_mov_b64 vcc, s[28:29]
	s_nop 0
	v_cndmask_b32_dpp v130, v60, v128, vcc quad_perm:[1,0,3,2] row_mask:0xf bank_mask:0xf
	v_cndmask_b32_dpp v131, v61, v129, vcc quad_perm:[1,0,3,2] row_mask:0xf bank_mask:0xf
	s_mov_b64 vcc, s[30:31]
	s_nop 0
	v_cndmask_b32_dpp v132, v128, v60, vcc quad_perm:[1,0,3,2] row_mask:0xf bank_mask:0xf
	v_cndmask_b32_dpp v133, v129, v61, vcc quad_perm:[1,0,3,2] row_mask:0xf bank_mask:0xf
	global_store_dwordx4 v[136:137], v[130:133], off sc0 sc1 nt
	s_nop 1
	s_waitcnt vmcnt(12)
	s_waitcnt lgkmcnt(0)
	s_barrier
	v_accvgpr_read_b32 v2, a1
	v_accvgpr_read_b32 v12, a5
	ds_read_b64 v[60:61], v12
	ds_read_b64 v[62:63], v12 offset:288
	ds_read_b64 v[68:69], v12 offset:576
	ds_read_b64 v[70:71], v12 offset:1728
	ds_read_b64 v[72:73], v12 offset:2016
	ds_read_b64 v[82:83], v12 offset:2304
	ds_read_b64 v[80:81], v12 offset:3456
	ds_read_b64 v[84:85], v12 offset:3744
	ds_read_b64 v[116:117], v12 offset:4032
	ds_read_b64 v[114:115], v12 offset:5184
	ds_read_b64 v[112:113], v12 offset:5472
	ds_read_b64 v[90:91], v12 offset:5760
	ds_read_b32 v43, v2
	ds_read_b32 v19, v2 offset:288
	ds_read_b32 v39, v2 offset:576
	ds_read_b32 v25, v2 offset:1728
	ds_read_b32 v7, v2 offset:2016
	ds_read_b32 v21, v2 offset:2304
	ds_read_b32 v11, v2 offset:3456
	ds_read_b32 v35, v2 offset:3744
	ds_read_b32 v59, v2 offset:4032
	ds_read_b32 v57, v2 offset:5184
	ds_read_b32 v51, v2 offset:5472
	ds_read_b32 v49, v2 offset:5760
	s_waitcnt lgkmcnt(0)
	v_accvgpr_read_b32 v101, a23
	v_mov_b32_e32 v46, v43
	v_mov_b32_e32 v65, v61
	v_accvgpr_read_b32 v31, a25
	v_mov_b32_dpp v46, v61 row_shr:1 row_mask:0xf bank_mask:0xf
	v_pk_mul_f32 v[86:87], v[64:65], v[46:47]
	v_accvgpr_read_b32 v100, a22
	v_accvgpr_read_b32 v30, a24
	v_mov_b32_e32 v26, v19
	v_mov_b32_dpp v43, v60 row_shl:1 row_mask:0xf bank_mask:0xf
	v_pk_fma_f32 v[86:87], v[60:61], v[100:101], v[86:87] op_sel_hi:[0,1,1]
	v_pk_mov_b32 v[60:61], v[60:61], v[30:31] op_sel:[1,0]
	v_mov_b32_dpp v26, v63 row_shr:1 row_mask:0xf bank_mask:0xf
	v_mov_b32_e32 v1, v63
	v_pk_fma_f32 v[60:61], v[60:61], v[42:43], v[86:87]
	v_pk_mul_f32 v[86:87], v[0:1], v[26:27]
	v_accvgpr_read_b32 v0, a34
	v_accvgpr_mov_b32 a12, a14
	v_accvgpr_read_b32 v1, a35
	v_accvgpr_mov_b32 a13, a15
	v_mov_b32_dpp v19, v62 row_shl:1 row_mask:0xf bank_mask:0xf
	v_pk_fma_f32 v[86:87], v[62:63], v[16:17], v[86:87] op_sel_hi:[0,1,1]
	v_accvgpr_write_b32 a14, v16
	v_pk_mov_b32 v[62:63], v[62:63], v[0:1] op_sel:[1,0]
	v_mov_b32_e32 v44, v39
	v_accvgpr_write_b32 a15, v17
	v_pk_fma_f32 v[62:63], v[62:63], v[18:19], v[86:87]
	v_pk_add_f32 v[60:61], v[60:61], 0 op_sel_hi:[1,0]
	v_mov_b32_dpp v44, v69 row_shr:1 row_mask:0xf bank_mask:0xf
	v_accvgpr_read_b32 v16, a48
	v_mov_b32_e32 v17, v69
	v_accvgpr_read_b32 v67, a47
	v_pk_add_f32 v[60:61], v[60:61], v[62:63]
	v_pk_mul_f32 v[62:63], v[16:17], v[44:45]
	v_accvgpr_read_b32 v66, a46
	v_mov_b32_dpp v39, v68 row_shl:1 row_mask:0xf bank_mask:0xf
	v_pk_fma_f32 v[62:63], v[68:69], v[14:15], v[62:63] op_sel_hi:[0,1,1]
	v_pk_mov_b32 v[68:69], v[68:69], v[66:67] op_sel:[1,0]
	v_mov_b32_e32 v36, v25
	v_pk_fma_f32 v[62:63], v[68:69], v[38:39], v[62:63]
	s_mov_b64 s[0:1], 0x1800000
	v_pk_add_f32 v[60:61], v[60:61], v[62:63]
	v_mov_b32_dpp v36, v71 row_shr:1 row_mask:0xf bank_mask:0xf
	v_mov_b32_e32 v127, v71
	v_lshl_add_u64 v[62:63], v[54:55], 0, s[0:1]
	v_mov_b32_e32 v128, v60
	v_mov_b32_e32 v129, v61
	v_pk_mul_f32 v[60:61], v[126:127], v[36:37]
	v_mov_b32_e32 v12, v7
	v_mov_b32_dpp v25, v70 row_shl:1 row_mask:0xf bank_mask:0xf
	v_pk_fma_f32 v[60:61], v[70:71], v[8:9], v[60:61] op_sel_hi:[0,1,1]
	v_mov_b32_e32 v62, v71
	v_mov_b32_e32 v63, v31
	v_mov_b32_dpp v12, v73 row_shr:1 row_mask:0xf bank_mask:0xf
	v_mov_b32_e32 v75, v73
	v_pk_fma_f32 v[60:61], v[62:63], v[24:25], v[60:61]
	v_pk_mul_f32 v[62:63], v[74:75], v[12:13]
	v_mov_b32_dpp v7, v72 row_shl:1 row_mask:0xf bank_mask:0xf
	v_pk_fma_f32 v[62:63], v[72:73], v[22:23], v[62:63] op_sel_hi:[0,1,1]
	v_accvgpr_write_b32 a4, v22
	v_mov_b32_e32 v68, v73
	v_mov_b32_e32 v69, v1
	v_mov_b32_e32 v78, v21
	v_accvgpr_write_b32 a5, v23
	v_pk_fma_f32 v[62:63], v[68:69], v[6:7], v[62:63]
	v_pk_add_f32 v[60:61], v[60:61], 0 op_sel_hi:[1,0]
	v_mov_b32_dpp v78, v83 row_shr:1 row_mask:0xf bank_mask:0xf
	v_mov_b32_e32 v53, v83
	v_accvgpr_read_b32 v22, a26
	v_pk_add_f32 v[60:61], v[60:61], v[62:63]
	v_pk_mul_f32 v[62:63], v[52:53], v[78:79]
	v_accvgpr_read_b32 v23, a27
	v_mov_b32_dpp v21, v82 row_shl:1 row_mask:0xf bank_mask:0xf
	v_pk_fma_f32 v[62:63], v[82:83], v[22:23], v[62:63] op_sel_hi:[0,1,1]
	v_mov_b32_e32 v68, v83
	v_mov_b32_e32 v69, v67
	v_pk_fma_f32 v[62:63], v[68:69], v[20:21], v[62:63]
	v_mov_b32_e32 v76, v11
	v_pk_add_f32 v[60:61], v[60:61], v[62:63]
	s_mov_b64 s[0:1], 0x1810000
	v_mov_b32_dpp v76, v81 row_shr:1 row_mask:0xf bank_mask:0xf
	v_mov_b32_e32 v121, v81
	v_accvgpr_read_b32 v15, a13
	v_lshl_add_u64 v[136:137], v[134:135], 0, s[0:1]
	s_nop 1
	s_mov_b64 vcc, s[28:29]
	s_nop 0
	v_cndmask_b32_dpp v130, v60, v128, vcc quad_perm:[1,0,3,2] row_mask:0xf bank_mask:0xf
	v_cndmask_b32_dpp v131, v61, v129, vcc quad_perm:[1,0,3,2] row_mask:0xf bank_mask:0xf
	s_mov_b64 vcc, s[30:31]
	s_nop 0
	v_cndmask_b32_dpp v132, v128, v60, vcc quad_perm:[1,0,3,2] row_mask:0xf bank_mask:0xf
	v_cndmask_b32_dpp v133, v129, v61, vcc quad_perm:[1,0,3,2] row_mask:0xf bank_mask:0xf
	global_store_dwordx4 v[136:137], v[130:133], off sc0 sc1 nt
	s_nop 1
	v_pk_mul_f32 v[60:61], v[120:121], v[76:77]
	v_accvgpr_read_b32 v14, a12
	v_mov_b32_e32 v2, v35
	v_mov_b32_dpp v11, v80 row_shl:1 row_mask:0xf bank_mask:0xf
	v_pk_fma_f32 v[60:61], v[80:81], v[124:125], v[60:61] op_sel_hi:[0,1,1]
	v_pk_mov_b32 v[62:63], v[80:81], v[14:15] op_sel:[1,0]
	v_mov_b32_dpp v2, v85 row_shr:1 row_mask:0xf bank_mask:0xf
	v_mov_b32_e32 v107, v85
	v_pk_fma_f32 v[60:61], v[62:63], v[10:11], v[60:61]
	v_pk_mul_f32 v[62:63], v[106:107], v[2:3]
	v_mov_b32_dpp v35, v84 row_shl:1 row_mask:0xf bank_mask:0xf
	v_pk_fma_f32 v[62:63], v[84:85], v[28:29], v[62:63] op_sel_hi:[0,1,1]
	v_pk_mov_b32 v[68:69], v[84:85], v[122:123] op_sel:[1,0]
	v_mov_b32_e32 v92, v59
	v_pk_fma_f32 v[62:63], v[68:69], v[34:35], v[62:63]
	v_pk_add_f32 v[60:61], v[60:61], 0 op_sel_hi:[1,0]
	v_mov_b32_dpp v92, v117 row_shr:1 row_mask:0xf bank_mask:0xf
	v_mov_b32_e32 v97, v117
	v_accvgpr_read_b32 v87, a9
	v_pk_add_f32 v[60:61], v[60:61], v[62:63]
	v_pk_mul_f32 v[62:63], v[96:97], v[92:93]
	v_accvgpr_read_b32 v86, a8
	v_mov_b32_dpp v59, v116 row_shl:1 row_mask:0xf bank_mask:0xf
	v_pk_fma_f32 v[62:63], v[116:117], v[86:87], v[62:63] op_sel_hi:[0,1,1]
	v_pk_mov_b32 v[68:69], v[116:117], v[118:119] op_sel:[1,0]
	v_mov_b32_e32 v94, v57
	v_pk_fma_f32 v[62:63], v[68:69], v[58:59], v[62:63]
	s_mov_b64 s[0:1], 0x1820000
	v_pk_add_f32 v[60:61], v[60:61], v[62:63]
	v_mov_b32_dpp v94, v115 row_shr:1 row_mask:0xf bank_mask:0xf
	v_mov_b32_e32 v99, v115
	v_lshl_add_u64 v[62:63], v[54:55], 0, s[0:1]
	v_mov_b32_e32 v128, v60
	v_mov_b32_e32 v129, v61
	v_pk_mul_f32 v[60:61], v[98:99], v[94:95]
	v_mov_b32_e32 v102, v51
	v_mov_b32_dpp v57, v114 row_shl:1 row_mask:0xf bank_mask:0xf
	v_pk_fma_f32 v[60:61], v[114:115], v[40:41], v[60:61] op_sel_hi:[0,1,1]
	v_mov_b32_e32 v62, v115
	v_mov_b32_e32 v63, v15
	v_mov_b32_dpp v102, v113 row_shr:1 row_mask:0xf bank_mask:0xf
	v_mov_b32_e32 v105, v113
	v_accvgpr_read_b32 v89, a19
	v_pk_fma_f32 v[60:61], v[62:63], v[56:57], v[60:61]
	v_pk_mul_f32 v[62:63], v[104:105], v[102:103]
	v_accvgpr_read_b32 v88, a18
	v_mov_b32_dpp v51, v112 row_shl:1 row_mask:0xf bank_mask:0xf
	v_pk_fma_f32 v[62:63], v[112:113], v[88:89], v[62:63] op_sel_hi:[0,1,1]
	v_mov_b32_e32 v68, v113
	v_mov_b32_e32 v69, v123
	v_mov_b32_e32 v108, v49
	v_pk_fma_f32 v[62:63], v[68:69], v[50:51], v[62:63]
	v_pk_add_f32 v[60:61], v[60:61], 0 op_sel_hi:[1,0]
	v_mov_b32_dpp v108, v91 row_shr:1 row_mask:0xf bank_mask:0xf
	v_mov_b32_e32 v111, v91
	v_pk_add_f32 v[60:61], v[60:61], v[62:63]
	v_pk_mul_f32 v[62:63], v[110:111], v[108:109]
	v_mov_b32_dpp v49, v90 row_shl:1 row_mask:0xf bank_mask:0xf
	v_pk_fma_f32 v[62:63], v[90:91], v[4:5], v[62:63] op_sel_hi:[0,1,1]
	v_mov_b32_e32 v68, v91
	v_mov_b32_e32 v69, v119
	v_pk_fma_f32 v[62:63], v[68:69], v[48:49], v[62:63]
	s_mov_b64 s[0:1], 0x1830000
	v_pk_add_f32 v[60:61], v[60:61], v[62:63]
	v_lshl_add_u64 v[136:137], v[134:135], 0, s[0:1]
	s_nop 1
	s_mov_b64 vcc, s[28:29]
	s_nop 0
	v_cndmask_b32_dpp v130, v60, v128, vcc quad_perm:[1,0,3,2] row_mask:0xf bank_mask:0xf
	v_cndmask_b32_dpp v131, v61, v129, vcc quad_perm:[1,0,3,2] row_mask:0xf bank_mask:0xf
	s_mov_b64 vcc, s[30:31]
	s_nop 0
	v_cndmask_b32_dpp v132, v128, v60, vcc quad_perm:[1,0,3,2] row_mask:0xf bank_mask:0xf
	v_cndmask_b32_dpp v133, v129, v61, vcc quad_perm:[1,0,3,2] row_mask:0xf bank_mask:0xf
	global_store_dwordx4 v[136:137], v[130:133], off sc0 sc1 nt
	s_nop 1
	v_accvgpr_write_b32 a12, v28
	s_waitcnt vmcnt(8)
	v_accvgpr_write_b32 a13, v29
	v_mov_b64_e32 v[28:29], v[4:5]
	s_waitcnt lgkmcnt(0)
	s_barrier
	v_accvgpr_read_b32 v2, a6
	v_accvgpr_read_b32 v4, a7
	ds_read_b64 v[60:61], v2
	ds_read_b64 v[62:63], v2 offset:288
	ds_read_b64 v[68:69], v2 offset:576
	ds_read_b64 v[70:71], v2 offset:1728
	ds_read_b64 v[72:73], v2 offset:2016
	ds_read_b64 v[82:83], v2 offset:2304
	ds_read_b64 v[80:81], v2 offset:3456
	ds_read_b64 v[84:85], v2 offset:3744
	ds_read_b64 v[116:117], v2 offset:4032
	ds_read_b64 v[114:115], v2 offset:5184
	ds_read_b64 v[112:113], v2 offset:5472
	ds_read_b64 v[90:91], v2 offset:5760
	ds_read_b32 v43, v4
	ds_read_b32 v19, v4 offset:288
	ds_read_b32 v39, v4 offset:576
	ds_read_b32 v25, v4 offset:1728
	ds_read_b32 v7, v4 offset:2016
	ds_read_b32 v21, v4 offset:2304
	ds_read_b32 v11, v4 offset:3456
	ds_read_b32 v35, v4 offset:3744
	ds_read_b32 v59, v4 offset:4032
	ds_read_b32 v57, v4 offset:5184
	ds_read_b32 v51, v4 offset:5472
	ds_read_b32 v49, v4 offset:5760
	s_waitcnt lgkmcnt(0)
	v_accvgpr_read_b32 v8, a24
	v_mov_b32_e32 v46, v43
	v_mov_b32_e32 v65, v61
	v_mov_b32_e32 v26, v19
	v_mov_b32_dpp v46, v61 row_shr:1 row_mask:0xf bank_mask:0xf
	v_accvgpr_read_b32 v32, a32
	v_accvgpr_read_b32 v9, a25
	v_mov_b64_e32 v[124:125], v[40:41]
	v_pk_mul_f32 v[30:31], v[64:65], v[46:47]
	v_mov_b32_dpp v26, v63 row_shr:1 row_mask:0xf bank_mask:0xf
	v_mov_b32_e32 v33, v63
	v_accvgpr_read_b32 v4, a14
	v_accvgpr_read_b32 v41, a35
	v_mov_b32_e32 v44, v39
	v_pk_fma_f32 v[30:31], v[60:61], v[100:101], v[30:31] op_sel_hi:[0,1,1]
	v_mov_b32_dpp v43, v60 row_shl:1 row_mask:0xf bank_mask:0xf
	v_pk_mov_b32 v[46:47], v[60:61], v[8:9] op_sel:[1,0]
	v_pk_mul_f32 v[26:27], v[32:33], v[26:27]
	v_accvgpr_read_b32 v5, a15
	v_accvgpr_read_b32 v40, a34
	v_mov_b32_dpp v44, v69 row_shr:1 row_mask:0xf bank_mask:0xf
	v_mov_b32_e32 v17, v69
	v_accvgpr_read_b32 v0, a16
	v_pk_fma_f32 v[30:31], v[46:47], v[42:43], v[30:31]
	v_pk_fma_f32 v[26:27], v[62:63], v[4:5], v[26:27] op_sel_hi:[0,1,1]
	v_mov_b32_dpp v19, v62 row_shl:1 row_mask:0xf bank_mask:0xf
	v_pk_mov_b32 v[32:33], v[62:63], v[40:41] op_sel:[1,0]
	v_pk_mul_f32 v[16:17], v[16:17], v[44:45]
	v_accvgpr_read_b32 v1, a17
	v_pk_fma_f32 v[18:19], v[32:33], v[18:19], v[26:27]
	v_pk_add_f32 v[26:27], v[30:31], 0 op_sel_hi:[1,0]
	v_mov_b32_dpp v39, v68 row_shl:1 row_mask:0xf bank_mask:0xf
	v_pk_fma_f32 v[16:17], v[68:69], v[0:1], v[16:17] op_sel_hi:[0,1,1]
	v_pk_mov_b32 v[30:31], v[68:69], v[66:67] op_sel:[1,0]
	v_pk_add_f32 v[18:19], v[26:27], v[18:19]
	v_pk_fma_f32 v[16:17], v[30:31], v[38:39], v[16:17]
	v_mov_b32_e32 v36, v25
	s_mov_b64 s[0:1], 0x1c00000
	v_pk_add_f32 v[16:17], v[18:19], v[16:17]
	v_mov_b32_dpp v36, v71 row_shr:1 row_mask:0xf bank_mask:0xf
	v_mov_b32_e32 v127, v71
	v_accvgpr_read_b32 v0, a20
	v_lshl_add_u64 v[26:27], v[54:55], 0, s[0:1]
	v_mov_b32_e32 v128, v16
	v_mov_b32_e32 v129, v17
	v_mov_b32_e32 v12, v7
	v_pk_mul_f32 v[16:17], v[126:127], v[36:37]
	v_accvgpr_read_b32 v1, a21
	v_mov_b32_dpp v12, v73 row_shr:1 row_mask:0xf bank_mask:0xf
	v_pk_fma_f32 v[16:17], v[70:71], v[0:1], v[16:17] op_sel_hi:[0,1,1]
	v_mov_b32_e32 v75, v73
	v_accvgpr_read_b32 v0, a4
	v_mov_b32_e32 v78, v21
	v_pk_mul_f32 v[12:13], v[74:75], v[12:13]
	v_accvgpr_read_b32 v1, a5
	v_mov_b32_dpp v25, v70 row_shl:1 row_mask:0xf bank_mask:0xf
	v_mov_b32_dpp v7, v72 row_shl:1 row_mask:0xf bank_mask:0xf
	v_mov_b32_dpp v78, v83 row_shr:1 row_mask:0xf bank_mask:0xf
	v_mov_b32_e32 v8, v71
	v_pk_fma_f32 v[12:13], v[72:73], v[0:1], v[12:13] op_sel_hi:[0,1,1]
	v_mov_b32_e32 v5, v41
	v_mov_b32_e32 v4, v73
	v_mov_b32_e32 v53, v83
	v_pk_fma_f32 v[16:17], v[8:9], v[24:25], v[16:17]
	v_pk_fma_f32 v[6:7], v[4:5], v[6:7], v[12:13]
	v_pk_mul_f32 v[12:13], v[52:53], v[78:79]
	v_mov_b32_dpp v21, v82 row_shl:1 row_mask:0xf bank_mask:0xf
	v_pk_add_f32 v[16:17], v[16:17], 0 op_sel_hi:[1,0]
	v_pk_fma_f32 v[12:13], v[82:83], v[22:23], v[12:13] op_sel_hi:[0,1,1]
	v_mov_b32_e32 v66, v83
	v_pk_add_f32 v[6:7], v[16:17], v[6:7]
	v_pk_fma_f32 v[12:13], v[66:67], v[20:21], v[12:13]
	v_mov_b32_e32 v76, v11
	v_pk_add_f32 v[6:7], v[6:7], v[12:13]
	s_mov_b64 s[0:1], 0x1c10000
	v_mov_b32_dpp v76, v81 row_shr:1 row_mask:0xf bank_mask:0xf
	v_mov_b32_e32 v121, v81
	v_accvgpr_read_b32 v0, a36
	v_lshl_add_u64 v[136:137], v[134:135], 0, s[0:1]
	s_nop 1
	s_mov_b64 vcc, s[28:29]
	s_nop 0
	v_cndmask_b32_dpp v130, v6, v128, vcc quad_perm:[1,0,3,2] row_mask:0xf bank_mask:0xf
	v_cndmask_b32_dpp v131, v7, v129, vcc quad_perm:[1,0,3,2] row_mask:0xf bank_mask:0xf
	s_mov_b64 vcc, s[30:31]
	s_nop 0
	v_cndmask_b32_dpp v132, v128, v6, vcc quad_perm:[1,0,3,2] row_mask:0xf bank_mask:0xf
	v_cndmask_b32_dpp v133, v129, v7, vcc quad_perm:[1,0,3,2] row_mask:0xf bank_mask:0xf
	global_store_dwordx4 v[136:137], v[130:133], off
	s_nop 1
	v_mov_b32_e32 v2, v35
	v_pk_mul_f32 v[6:7], v[120:121], v[76:77]
	v_accvgpr_read_b32 v1, a37
	v_mov_b32_dpp v2, v85 row_shr:1 row_mask:0xf bank_mask:0xf
	v_pk_fma_f32 v[6:7], v[80:81], v[0:1], v[6:7] op_sel_hi:[0,1,1]
	v_mov_b32_e32 v107, v85
	v_accvgpr_read_b32 v0, a12
	v_mov_b32_e32 v92, v59
	v_pk_mul_f32 v[2:3], v[106:107], v[2:3]
	v_accvgpr_read_b32 v1, a13
	v_mov_b32_dpp v11, v80 row_shl:1 row_mask:0xf bank_mask:0xf
	v_mov_b32_dpp v35, v84 row_shl:1 row_mask:0xf bank_mask:0xf
	v_mov_b32_dpp v92, v117 row_shr:1 row_mask:0xf bank_mask:0xf
	v_pk_mov_b32 v[8:9], v[80:81], v[14:15] op_sel:[1,0]
	v_pk_fma_f32 v[2:3], v[84:85], v[0:1], v[2:3] op_sel_hi:[0,1,1]
	v_pk_mov_b32 v[4:5], v[84:85], v[122:123] op_sel:[1,0]
	v_mov_b32_e32 v97, v117
	v_pk_fma_f32 v[6:7], v[8:9], v[10:11], v[6:7]
	v_pk_fma_f32 v[0:1], v[4:5], v[34:35], v[2:3]
	v_pk_mul_f32 v[2:3], v[96:97], v[92:93]
	v_mov_b32_dpp v59, v116 row_shl:1 row_mask:0xf bank_mask:0xf
	v_pk_add_f32 v[6:7], v[6:7], 0 op_sel_hi:[1,0]
	v_pk_fma_f32 v[2:3], v[116:117], v[86:87], v[2:3] op_sel_hi:[0,1,1]
	v_pk_mov_b32 v[4:5], v[116:117], v[118:119] op_sel:[1,0]
	v_pk_add_f32 v[0:1], v[6:7], v[0:1]
	v_pk_fma_f32 v[2:3], v[4:5], v[58:59], v[2:3]
	v_mov_b32_e32 v94, v57
	v_pk_add_f32 v[0:1], v[0:1], v[2:3]
	s_mov_b64 s[0:1], 0x1c20000
	v_mov_b32_dpp v94, v115 row_shr:1 row_mask:0xf bank_mask:0xf
	v_mov_b32_e32 v102, v51
	v_mov_b32_e32 v99, v115
	v_lshl_add_u64 v[2:3], v[54:55], 0, s[0:1]
	v_mov_b32_e32 v128, v0
	v_mov_b32_e32 v129, v1
	v_mov_b32_dpp v102, v113 row_shr:1 row_mask:0xf bank_mask:0xf
	v_pk_mul_f32 v[0:1], v[98:99], v[94:95]
	v_mov_b32_e32 v105, v113
	v_mov_b32_dpp v57, v114 row_shl:1 row_mask:0xf bank_mask:0xf
	v_pk_fma_f32 v[0:1], v[114:115], v[124:125], v[0:1] op_sel_hi:[0,1,1]
	v_mov_b32_e32 v14, v115
	v_pk_mul_f32 v[2:3], v[104:105], v[102:103]
	v_mov_b32_dpp v51, v112 row_shl:1 row_mask:0xf bank_mask:0xf
	v_mov_b32_e32 v108, v49
	v_pk_fma_f32 v[0:1], v[14:15], v[56:57], v[0:1]
	v_pk_fma_f32 v[2:3], v[112:113], v[88:89], v[2:3] op_sel_hi:[0,1,1]
	v_mov_b32_e32 v122, v113
	v_mov_b32_dpp v108, v91 row_shr:1 row_mask:0xf bank_mask:0xf
	v_pk_add_f32 v[0:1], v[0:1], 0 op_sel_hi:[1,0]
	v_pk_fma_f32 v[2:3], v[122:123], v[50:51], v[2:3]
	v_mov_b32_e32 v111, v91
	v_pk_add_f32 v[0:1], v[0:1], v[2:3]
	v_pk_mul_f32 v[2:3], v[110:111], v[108:109]
	v_mov_b32_dpp v49, v90 row_shl:1 row_mask:0xf bank_mask:0xf
	v_pk_fma_f32 v[2:3], v[90:91], v[28:29], v[2:3] op_sel_hi:[0,1,1]
	v_mov_b32_e32 v118, v91
	v_pk_fma_f32 v[2:3], v[118:119], v[48:49], v[2:3]
	s_mov_b64 s[0:1], 0x1c30000
	v_pk_add_f32 v[0:1], v[0:1], v[2:3]
	v_lshl_add_u64 v[136:137], v[134:135], 0, s[0:1]
	s_nop 1
	s_mov_b64 vcc, s[28:29]
	s_nop 0
	v_cndmask_b32_dpp v130, v0, v128, vcc quad_perm:[1,0,3,2] row_mask:0xf bank_mask:0xf
	v_cndmask_b32_dpp v131, v1, v129, vcc quad_perm:[1,0,3,2] row_mask:0xf bank_mask:0xf
	s_mov_b64 vcc, s[30:31]
	s_nop 0
	v_cndmask_b32_dpp v132, v128, v0, vcc quad_perm:[1,0,3,2] row_mask:0xf bank_mask:0xf
	v_cndmask_b32_dpp v133, v129, v1, vcc quad_perm:[1,0,3,2] row_mask:0xf bank_mask:0xf
	global_store_dwordx4 v[136:137], v[130:133], off
	s_nop 1
	s_endpgm
